# attention QK: all K-fragment LDS reads of a block issued together into spare VGPR quads, MFMAs behind counted lgkmcnt waits
# speedup vs baseline: 1.0042x; 1.0019x over previous
.LBB0_507:
	ds_read_b128 v[72:75], v191 offset:18432
	ds_read_b128 v[80:83], v191 offset:18496
	ds_read_b128 v[224:227], v191 offset:20736
	ds_read_b128 v[228:231], v191 offset:20800
	ds_read_b128 v[232:235], v191 offset:23040
	ds_read_b128 v[236:239], v191 offset:23104
	ds_read_b128 v[240:243], v191 offset:25344
	ds_read_b128 v[244:247], v191 offset:25408
	s_waitcnt lgkmcnt(7)
	v_mfma_f32_16x16x32_bf16 v[52:55], v[72:75], v[4:7], v[52:55]
	v_mfma_f32_16x16x32_bf16 v[72:75], v[72:75], v[12:15], v[56:59]
	s_waitcnt lgkmcnt(6)
	v_mfma_f32_16x16x32_bf16 v[56:59], v[80:83], v[8:11], v[52:55]
	s_nop 4
	s_waitcnt lgkmcnt(5)
	v_mfma_f32_16x16x32_bf16 v[44:47], v[224:227], v[4:7], v[44:47]
	v_mfma_f32_16x16x32_bf16 v[52:55], v[224:227], v[12:15], v[64:67]
	s_nop 2
	v_mfma_f32_16x16x32_bf16 v[72:75], v[80:83], v[16:19], v[72:75]
	s_waitcnt lgkmcnt(4)
	v_mfma_f32_16x16x32_bf16 v[80:83], v[228:231], v[16:19], v[52:55]
	s_nop 2
	v_mfma_f32_16x16x32_bf16 v[44:47], v[228:231], v[8:11], v[44:47]
	s_waitcnt lgkmcnt(3)
	v_mfma_f32_16x16x32_bf16 v[60:63], v[232:235], v[4:7], v[60:63]
	v_mfma_f32_16x16x32_bf16 v[52:55], v[232:235], v[12:15], v[84:87]
	s_waitcnt lgkmcnt(2)
	v_mfma_f32_16x16x32_bf16 v[84:87], v[236:239], v[16:19], v[52:55]
	v_mfma_f32_16x16x32_bf16 v[148:151], v[236:239], v[8:11], v[60:63]
	s_nop 4
	s_waitcnt lgkmcnt(1)
	v_mfma_f32_16x16x32_bf16 v[48:51], v[240:243], v[4:7], v[48:51]
	v_mfma_f32_16x16x32_bf16 v[52:55], v[240:243], v[12:15], v[100:103]
	s_waitcnt lgkmcnt(0)
	v_mfma_f32_16x16x32_bf16 v[154:157], v[244:247], v[8:11], v[48:51]
	s_nop 4
	v_max_f32_e32 v3, v58, v59
	v_max_f32_e32 v48, v46, v47
	v_max_f32_e32 v49, v148, v149
	v_mfma_f32_16x16x32_bf16 v[100:103], v[244:247], v[16:19], v[52:55]
	v_max_f32_e32 v50, v150, v151
	v_max3_f32 v3, v56, v57, v3
	v_max_f32_e32 v51, v156, v157
	v_max3_f32 v51, v154, v155, v51
	v_max3_f32 v48, v44, v45, v48
	v_max3_f32 v49, v49, v50, v51
	v_max3_f32 v3, v3, v48, v49
	v_mov_b32_e32 v48, v3
	s_nop 1
	v_permlane32_swap_b32_e32 v3, v48
	v_max_f32_e32 v3, v3, v48
	v_mov_b32_e32 v48, v3
	s_nop 1
	v_permlane16_swap_b32_e32 v3, v48
	v_max3_f32 v218, v220, v3, v48
	v_sub_f32_e32 v3, v220, v218
	v_exp_f32_e32 v128, v3
	v_sub_f32_e32 v3, v56, v218
	v_pk_mul_f32 v[52:53], v[104:105], v[128:129] op_sel_hi:[1,0]
	v_exp_f32_e32 v105, v3
	v_sub_f32_e32 v3, v57, v218
	v_pk_mul_f32 v[54:55], v[106:107], v[128:129] op_sel_hi:[1,0]
	v_exp_f32_e32 v107, v3
	v_sub_f32_e32 v3, v58, v218
	v_pk_mul_f32 v[48:49], v[112:113], v[128:129] op_sel_hi:[1,0]
	v_exp_f32_e32 v113, v3
	v_sub_f32_e32 v3, v59, v218
	v_pk_mul_f32 v[50:51], v[114:115], v[128:129] op_sel_hi:[1,0]
	v_exp_f32_e32 v115, v3
	v_sub_f32_e32 v3, v44, v218
	v_exp_f32_e32 v133, v3
	v_sub_f32_e32 v3, v45, v218
	v_exp_f32_e32 v137, v3
	v_sub_f32_e32 v3, v46, v218
	v_exp_f32_e32 v139, v3
	v_sub_f32_e32 v3, v47, v218
	v_exp_f32_e32 v147, v3
	v_sub_f32_e32 v3, v148, v218
	v_exp_f32_e32 v135, v3
	v_sub_f32_e32 v3, v149, v218
	v_exp_f32_e32 v141, v3
	v_sub_f32_e32 v3, v150, v218
	v_exp_f32_e32 v143, v3
	v_sub_f32_e32 v3, v151, v218
	v_exp_f32_e32 v149, v3
	v_sub_f32_e32 v3, v154, v218
	v_exp_f32_e32 v151, v3
	v_sub_f32_e32 v3, v155, v218
	v_exp_f32_e32 v153, v3
	v_sub_f32_e32 v3, v156, v218
	v_exp_f32_e32 v155, v3
	v_sub_f32_e32 v3, v157, v218
	v_pk_mul_f32 v[64:65], v[92:93], v[128:129] op_sel_hi:[1,0]
	v_exp_f32_e32 v157, v3
	v_max_f32_e32 v3, v74, v75
	v_pk_mul_f32 v[66:67], v[94:95], v[128:129] op_sel_hi:[1,0]
	v_max_f32_e32 v92, v82, v83
	v_max_f32_e32 v93, v84, v85
	v_pk_mul_f32 v[60:61], v[96:97], v[128:129] op_sel_hi:[1,0]
	v_max_f32_e32 v94, v86, v87
	v_max_f32_e32 v95, v102, v103
	v_max3_f32 v95, v100, v101, v95
	v_max3_f32 v3, v72, v73, v3
	v_max3_f32 v92, v80, v81, v92
	v_max3_f32 v93, v93, v94, v95
	v_max3_f32 v3, v3, v92, v93
	v_mov_b32_e32 v92, v3
	s_nop 1
	v_permlane32_swap_b32_e32 v3, v92
	v_max_f32_e32 v3, v3, v92
	v_mov_b32_e32 v92, v3
	s_nop 1
	v_permlane16_swap_b32_e32 v3, v92
	v_max3_f32 v217, v219, v3, v92
	v_sub_f32_e32 v3, v219, v217
	v_exp_f32_e32 v220, v3
	v_sub_f32_e32 v3, v72, v217
	v_exp_f32_e32 v104, v3
	v_sub_f32_e32 v3, v73, v217
	v_exp_f32_e32 v106, v3
	v_sub_f32_e32 v3, v74, v217
	v_exp_f32_e32 v112, v3
	v_sub_f32_e32 v3, v75, v217
	v_exp_f32_e32 v114, v3
	v_sub_f32_e32 v3, v80, v217
	v_exp_f32_e32 v132, v3
	v_sub_f32_e32 v3, v81, v217
	v_exp_f32_e32 v136, v3
	v_sub_f32_e32 v3, v82, v217
	v_exp_f32_e32 v138, v3
	v_sub_f32_e32 v3, v83, v217
	v_exp_f32_e32 v146, v3
	v_sub_f32_e32 v3, v84, v217
	v_exp_f32_e32 v134, v3
	v_sub_f32_e32 v3, v85, v217
	v_exp_f32_e32 v140, v3
	v_sub_f32_e32 v3, v86, v217
	v_exp_f32_e32 v142, v3
	v_sub_f32_e32 v3, v87, v217
	v_exp_f32_e32 v148, v3
	v_sub_f32_e32 v3, v100, v217
	v_exp_f32_e32 v150, v3
	v_sub_f32_e32 v3, v101, v217
	v_exp_f32_e32 v152, v3
	v_sub_f32_e32 v3, v102, v217
	v_exp_f32_e32 v154, v3
	v_sub_f32_e32 v3, v103, v217
	v_exp_f32_e32 v156, v3
	v_pk_mul_f32 v[94:95], v[78:79], v[220:221] op_sel_hi:[1,0]
	v_pk_mul_f32 v[92:93], v[76:77], v[220:221] op_sel_hi:[1,0]
	v_pk_add_f32 v[72:73], v[132:133], v[104:105]
	v_pk_add_f32 v[74:75], v[136:137], v[106:107]
	v_pk_add_f32 v[76:77], v[138:139], v[112:113]
	v_pk_add_f32 v[78:79], v[146:147], v[114:115]
	v_pk_add_f32 v[72:73], v[134:135], v[72:73]
	v_pk_add_f32 v[74:75], v[140:141], v[74:75]
	v_pk_add_f32 v[76:77], v[142:143], v[76:77]
	v_pk_add_f32 v[78:79], v[148:149], v[78:79]
	v_pk_add_f32 v[72:73], v[150:151], v[72:73]
	v_pk_add_f32 v[74:75], v[152:153], v[74:75]
	v_pk_add_f32 v[76:77], v[154:155], v[76:77]
	v_pk_add_f32 v[78:79], v[156:157], v[78:79]
	v_pk_add_f32 v[72:73], v[72:73], v[74:75]
	v_pk_add_f32 v[74:75], v[76:77], v[78:79]
	v_pk_mul_f32 v[62:63], v[98:99], v[128:129] op_sel_hi:[1,0]
	v_pk_mul_f32 v[98:99], v[70:71], v[220:221] op_sel_hi:[1,0]
	v_pk_mul_f32 v[96:97], v[68:69], v[220:221] op_sel_hi:[1,0]
	v_pk_mul_f32 v[90:91], v[90:91], v[220:221] op_sel_hi:[1,0]
	v_pk_mul_f32 v[88:89], v[88:89], v[220:221] op_sel_hi:[1,0]
	v_pk_mul_f32 v[70:71], v[110:111], v[220:221] op_sel_hi:[1,0]
	v_pk_mul_f32 v[68:69], v[108:109], v[220:221] op_sel_hi:[1,0]
	v_mov_b32_e32 v221, v128
	v_pk_add_f32 v[72:73], v[72:73], v[74:75]
	v_cvt_pk_bf16_f32 v56, v105, v107
	v_cvt_pk_bf16_f32 v57, v113, v115
	v_cvt_pk_bf16_f32 v58, v133, v137
	v_cvt_pk_bf16_f32 v59, v139, v147
	v_cvt_pk_bf16_f32 v44, v135, v141
	v_cvt_pk_bf16_f32 v45, v143, v149
	v_cvt_pk_bf16_f32 v46, v151, v153
	v_cvt_pk_bf16_f32 v47, v155, v157
	s_nop 0
	v_pk_fma_f32 v[128:129], v[130:131], v[220:221], v[72:73]
	v_cvt_pk_bf16_f32 v72, v104, v106
	v_cvt_pk_bf16_f32 v73, v112, v114
	v_cvt_pk_bf16_f32 v74, v132, v136
	v_cvt_pk_bf16_f32 v75, v138, v146
	v_cvt_pk_bf16_f32 v76, v134, v140
	v_cvt_pk_bf16_f32 v77, v142, v148
	v_cvt_pk_bf16_f32 v78, v150, v152
	v_cvt_pk_bf16_f32 v79, v154, v156
	ds_read_b64_tr_b16 v[82:83], v192 offset:29952
	ds_read_b64_tr_b16 v[80:81], v192 offset:27648
	ds_read_b64_tr_b16 v[84:85], v192 offset:27680
	ds_read_b64_tr_b16 v[86:87], v192 offset:29984
	s_waitcnt lgkmcnt(0)
	v_mfma_f32_16x16x32_bf16 v[60:63], v[84:87], v[56:59], v[60:63]
	v_mfma_f32_16x16x32_bf16 v[84:87], v[84:87], v[72:75], v[92:95]
	s_nop 2
	ds_read_b64_tr_b16 v[92:93], v192 offset:27712
	ds_read_b64_tr_b16 v[94:95], v192 offset:30016
	v_mfma_f32_16x16x32_bf16 v[64:67], v[80:83], v[56:59], v[64:67]
	v_mfma_f32_16x16x32_bf16 v[80:83], v[80:83], v[72:75], v[96:99]
	s_waitcnt lgkmcnt(0)
	v_mfma_f32_16x16x32_bf16 v[96:99], v[92:95], v[56:59], v[52:55]
	s_nop 2
	ds_read_b64_tr_b16 v[52:53], v192 offset:27744
	ds_read_b64_tr_b16 v[54:55], v192 offset:30048
	s_waitcnt lgkmcnt(0)
	v_mfma_f32_16x16x32_bf16 v[48:51], v[52:55], v[56:59], v[48:51]
	v_mfma_f32_16x16x32_bf16 v[68:71], v[52:55], v[72:75], v[68:71]
	ds_read_b64_tr_b16 v[54:55], v193 offset:29952
	ds_read_b64_tr_b16 v[52:53], v193 offset:27648
	ds_read_b64_tr_b16 v[56:57], v193 offset:27680
	ds_read_b64_tr_b16 v[58:59], v193 offset:29984
	v_mfma_f32_16x16x32_bf16 v[88:91], v[92:95], v[72:75], v[88:91]
	s_waitcnt lgkmcnt(2)
	v_mfma_f32_16x16x32_bf16 v[72:75], v[52:55], v[44:47], v[64:67]
	v_mfma_f32_16x16x32_bf16 v[52:55], v[52:55], v[76:79], v[80:83]
	s_waitcnt lgkmcnt(0)
	v_mfma_f32_16x16x32_bf16 v[80:83], v[56:59], v[44:47], v[60:63]
	s_nop 2
	ds_read_b64_tr_b16 v[60:61], v193 offset:27712
	ds_read_b64_tr_b16 v[62:63], v193 offset:30016
	ds_read_b64_tr_b16 v[64:65], v193 offset:27744
	ds_read_b64_tr_b16 v[66:67], v193 offset:30048
	v_mfma_f32_16x16x32_bf16 v[56:59], v[56:59], v[76:79], v[84:87]
	s_waitcnt lgkmcnt(2)
	v_mfma_f32_16x16x32_bf16 v[84:87], v[60:63], v[44:47], v[96:99]
	v_mfma_f32_16x16x32_bf16 v[60:63], v[60:63], v[76:79], v[88:91]
	s_waitcnt lgkmcnt(0)
	v_mfma_f32_16x16x32_bf16 v[100:103], v[64:67], v[44:47], v[48:51]
	v_mfma_f32_16x16x32_bf16 v[64:67], v[64:67], v[76:79], v[68:71]

; #define LAS __attribute__((address_space(3)))
; #define ATT_WRITE(buf_, kq_, vq_) do { const int key = F.tid >> 3, ds = (F.tid & 7) * 8; LAS bf16_t* Kd = Ks0 + (buf_) * 9216; LAS bf16_t* Vd = Kd + 4608; \
;             *(LAS u32x4*)(Kd + key * 72 + ds) = kq_; *(LAS u32x4*)(Vd + key * 72 + ds) = vq_; } while (0)
; __device__ __forceinline__ void ph_attn(const Frame& F, int j) {
;     ...
;         auto chunk = [&](const int ch, u32x4& kw, u32x4& vw, u32x4& kl, u32x4& vl) __attribute__((always_inline)) {
;             const bool loc = ch < nloc; const int kr = rlo + ch;
;             ATT_WRITE((ch + 1) & 1, kw, vw);
;             ATT_LOAD(kl, vl, ch + 4);
;             const LAS bf16_t* Ks = Ks0 + (ch & 1) * 9216; const LAS bf16_t* Vt = Ks + 4608;
;             const bool m0 = (ch < nch) && (loc ? (kr >= r0t[0] && kr < r0t[0] + 8) : true);
;             const bool m1 = (ch < nch) && (loc ? (kr >= r0t[1] && kr < r0t[1] + 8) : true);
;             if (m0 && m1) ATT_COMPUTE(3); else if (m0) ATT_COMPUTE(1); else if (m1) ATT_COMPUTE(2);
.LBB0_509:
	s_add_i32 s0, s30, -3
	v_mov_b32_e32 v44, s13
	v_cmp_lt_i32_e32 vcc, s0, v214
	v_min_i32_e32 v3, s0, v215
	v_mov_b32_e32 v45, s9
	v_cndmask_b32_e32 v44, v216, v44, vcc
	v_mov_b32_e32 v46, s26
	v_add_u32_e32 v3, v44, v3
	v_cndmask_b32_e32 v45, v45, v46, vcc
	v_lshlrev_b32_e32 v3, 6, v3
	v_add_u32_e32 v3, v3, v45
	v_add_u32_e32 v44, v3, v194
	v_ashrrev_i32_e32 v45, 31, v44
	v_lshlrev_b64 v[44:45], 13, v[44:45]
	v_lshl_add_u64 v[48:49], v[0:1], 0, v[44:45]
	global_load_dwordx4 v[44:47], v[48:49], off offset:1024
	s_nop 0
	global_load_dwordx4 v[48:51], v[48:49], off offset:2048
	s_add_i32 s54, s11, s30
	s_add_i32 s0, s30, -7
	s_add_i32 s2, s54, -11
	s_cmp_ge_u32 s2, s24
	v_cmp_ge_i32_e64 s[46:47], s0, v214
	v_cmp_lt_i32_e64 s[48:49], s0, v214
	s_cselect_b64 s[0:1], -1, 0
	s_cmp_lt_u32 s2, s27
	s_cselect_b64 s[4:5], -1, 0
	s_and_b64 s[0:1], s[0:1], s[4:5]
	s_or_b64 s[6:7], s[46:47], s[0:1]
	s_cmp_ge_u32 s2, s25
	s_cselect_b64 s[0:1], -1, 0
	s_cmp_lt_u32 s2, s28
	s_cselect_b64 s[4:5], -1, 0
	s_and_b64 s[0:1], s[0:1], s[4:5]
	s_or_b64 s[4:5], s[46:47], s[0:1]
	s_and_b64 s[0:1], s[6:7], s[4:5]
	s_andn2_b64 vcc, exec, s[0:1]
	s_mov_b64 s[0:1], -1
	s_waitcnt vmcnt(7)
	ds_write_b128 v196, v[28:31] offset:18432
	s_waitcnt vmcnt(6)
	ds_write_b128 v196, v[32:35] offset:27648
	s_cbranch_vccz .LBB0_525
	s_xor_b64 s[6:7], s[6:7], -1
	s_and_b64 vcc, exec, s[6:7]
	s_cbranch_vccz .LBB0_514
	v_mov_b64_e32 v[70:71], v[54:55]
	v_mov_b64_e32 v[78:79], v[58:59]
	v_mov_b64_e32 v[90:91], v[62:63]
	v_mov_b64_e32 v[110:111], v[66:67]
	s_andn2_b64 vcc, exec, s[4:5]
	v_mov_b64_e32 v[130:131], v[128:129]
	v_mov_b32_e32 v134, v217
	v_mov_b64_e32 v[68:69], v[52:53]
	v_mov_b64_e32 v[76:77], v[56:57]
	v_mov_b64_e32 v[88:89], v[60:61]
	v_mov_b64_e32 v[108:109], v[64:65]
	s_cbranch_vccnz .LBB0_513
	v_add_u32_e32 v3, s31, v198
	ds_read_b32 v28, v3 offset:37120
	v_add_u32_e32 v3, s31, v199
	ds_read_b32 v29, v3 offset:37120
	v_add_u32_e32 v3, s31, v200
	ds_read_b32 v30, v3 offset:37120
	v_add_u32_e32 v3, s31, v201
	ds_read_b32 v31, v3 offset:37120
	v_add_u32_e32 v3, s31, v202
	ds_read_b32 v32, v3 offset:37120
	v_add_u32_e32 v3, s31, v203
	ds_read_b32 v33, v3 offset:37120
	v_add_u32_e32 v3, s31, v204
	ds_read_b32 v34, v3 offset:37120
	v_add_u32_e32 v3, s31, v205
	ds_read_b32 v35, v3 offset:37120
	v_add_u32_e32 v3, s31, v206
	ds_read_b32 v68, v3 offset:37120
	v_add_u32_e32 v3, s31, v207
	ds_read_b32 v69, v3 offset:37120
	v_add_u32_e32 v3, s31, v208
	ds_read_b32 v70, v3 offset:37120
	v_add_u32_e32 v3, s31, v209
	ds_read_b32 v71, v3 offset:37120
	v_add_u32_e32 v3, s31, v210
	ds_read_b32 v76, v3 offset:37120
	v_add_u32_e32 v3, s31, v211
	ds_read_b32 v77, v3 offset:37120
	v_add_u32_e32 v3, s31, v212
	ds_read_b32 v78, v3 offset:37120
	v_add_u32_e32 v3, s31, v213
	ds_read_b32 v79, v3 offset:37120
	ds_read_b128 v[88:91], v191
	ds_read_b128 v[224:227], v191 offset:64
	ds_read_b128 v[228:231], v191 offset:2304
	ds_read_b128 v[232:235], v191 offset:2368
	ds_read_b128 v[236:239], v191 offset:4608
	ds_read_b128 v[240:243], v191 offset:4672
	ds_read_b128 v[244:247], v191 offset:6912
	ds_read_b128 v[182:185], v191 offset:6976
	s_waitcnt lgkmcnt(7)
	v_mfma_f32_16x16x32_bf16 v[28:31], v[88:91], v[12:15], v[28:31]
	v_mov_b32_e32 v131, v129
	s_waitcnt lgkmcnt(6)
	v_mfma_f32_16x16x32_bf16 v[28:31], v[224:227], v[16:19], v[28:31]
	s_nop 6
	s_waitcnt lgkmcnt(5)
	v_mfma_f32_16x16x32_bf16 v[32:35], v[228:231], v[12:15], v[32:35]
	s_waitcnt lgkmcnt(4)
	v_mfma_f32_16x16x32_bf16 v[32:35], v[232:235], v[16:19], v[32:35]
	s_waitcnt lgkmcnt(3)
	v_mfma_f32_16x16x32_bf16 v[68:71], v[236:239], v[12:15], v[68:71]
	s_waitcnt lgkmcnt(2)
	v_mfma_f32_16x16x32_bf16 v[68:71], v[240:243], v[16:19], v[68:71]
	s_waitcnt lgkmcnt(1)
	v_mfma_f32_16x16x32_bf16 v[76:79], v[244:247], v[12:15], v[76:79]
	s_waitcnt lgkmcnt(0)
	v_mfma_f32_16x16x32_bf16 v[76:79], v[182:185], v[16:19], v[76:79]
	v_max_f32_e32 v3, v30, v31
	v_max_f32_e32 v88, v34, v35
	s_nop 1
	v_max_f32_e32 v89, v68, v69
	v_max_f32_e32 v90, v70, v71
	s_nop 1
	v_max_f32_e32 v91, v78, v79
	v_max3_f32 v91, v76, v77, v91
	v_max3_f32 v3, v28, v29, v3
	v_max3_f32 v88, v32, v33, v88
	v_max3_f32 v89, v89, v90, v91
	v_max3_f32 v3, v3, v88, v89
	v_mov_b32_e32 v88, v3
	s_nop 1
	v_permlane32_swap_b32_e32 v3, v88
	v_max_f32_e32 v3, v3, v88
	v_mov_b32_e32 v88, v3
	s_nop 1
	v_permlane16_swap_b32_e32 v3, v88
	v_max3_f32 v134, v217, v3, v88
	v_sub_f32_e32 v3, v217, v134
	v_exp_f32_e32 v108, v3
	v_sub_f32_e32 v3, v28, v134
	v_exp_f32_e32 v28, v3
	v_sub_f32_e32 v3, v29, v134
	v_exp_f32_e32 v110, v3
	v_sub_f32_e32 v3, v30, v134
	v_exp_f32_e32 v29, v3
	v_sub_f32_e32 v3, v31, v134
	v_exp_f32_e32 v111, v3
	v_sub_f32_e32 v3, v32, v134
	v_exp_f32_e32 v30, v3
	v_sub_f32_e32 v3, v33, v134
	v_exp_f32_e32 v32, v3
	v_sub_f32_e32 v3, v34, v134
	v_exp_f32_e32 v31, v3
	v_sub_f32_e32 v3, v35, v134
	v_exp_f32_e32 v33, v3
	v_sub_f32_e32 v3, v68, v134
	v_exp_f32_e32 v34, v3
	v_sub_f32_e32 v3, v69, v134
	v_exp_f32_e32 v68, v3
	v_sub_f32_e32 v3, v70, v134
	v_exp_f32_e32 v35, v3
	v_sub_f32_e32 v3, v71, v134
	v_exp_f32_e32 v69, v3
	v_sub_f32_e32 v3, v76, v134
	v_exp_f32_e32 v70, v3
	v_sub_f32_e32 v3, v77, v134
	v_exp_f32_e32 v76, v3
	v_sub_f32_e32 v3, v78, v134
	v_exp_f32_e32 v71, v3
	v_sub_f32_e32 v3, v79, v134
	v_exp_f32_e32 v77, v3
	v_pk_add_f32 v[78:79], v[30:31], v[28:29]
	v_pk_add_f32 v[112:113], v[32:33], v[110:111]
	v_pk_add_f32 v[78:79], v[34:35], v[78:79]
	v_pk_add_f32 v[112:113], v[68:69], v[112:113]
	v_pk_add_f32 v[78:79], v[70:71], v[78:79]
	v_pk_add_f32 v[112:113], v[76:77], v[112:113]
	v_cvt_pk_bf16_f32 v28, v28, v110
	v_cvt_pk_bf16_f32 v29, v29, v111
	v_cvt_pk_bf16_f32 v30, v30, v32
	v_cvt_pk_bf16_f32 v31, v31, v33
	v_cvt_pk_bf16_f32 v32, v34, v68
	s_nop 0
	v_pk_add_f32 v[78:79], v[78:79], v[112:113]
	v_cvt_pk_bf16_f32 v33, v35, v69
	v_cvt_pk_bf16_f32 v34, v70, v76
	v_cvt_pk_bf16_f32 v35, v71, v77
	ds_read_b64_tr_b16 v[70:71], v192 offset:11520
	ds_read_b64_tr_b16 v[68:69], v192 offset:9216
	ds_read_b64_tr_b16 v[76:77], v192 offset:9248
	v_add_f32_e32 v130, v78, v79
	ds_read_b64_tr_b16 v[78:79], v192 offset:11552
	v_pk_mul_f32 v[90:91], v[54:55], v[108:109] op_sel_hi:[1,0]
	v_pk_mul_f32 v[88:89], v[52:53], v[108:109] op_sel_hi:[1,0]
	v_pk_mul_f32 v[94:95], v[58:59], v[108:109] op_sel_hi:[1,0]
	v_pk_mul_f32 v[92:93], v[56:57], v[108:109] op_sel_hi:[1,0]
	s_waitcnt lgkmcnt(2)
	v_mfma_f32_16x16x32_bf16 v[68:71], v[68:71], v[28:31], v[88:91]
	s_nop 2
	ds_read_b64_tr_b16 v[88:89], v192 offset:9280
	ds_read_b64_tr_b16 v[90:91], v192 offset:11584
	v_pk_mul_f32 v[98:99], v[62:63], v[108:109] op_sel_hi:[1,0]
	v_pk_mul_f32 v[96:97], v[60:61], v[108:109] op_sel_hi:[1,0]
	s_waitcnt lgkmcnt(2)
	v_mfma_f32_16x16x32_bf16 v[76:79], v[76:79], v[28:31], v[92:95]
	s_nop 2
	ds_read_b64_tr_b16 v[92:93], v192 offset:9312
	ds_read_b64_tr_b16 v[94:95], v192 offset:11616
	v_pk_mul_f32 v[106:107], v[66:67], v[108:109] op_sel_hi:[1,0]
	v_pk_mul_f32 v[104:105], v[64:65], v[108:109] op_sel_hi:[1,0]
	s_waitcnt lgkmcnt(2)
	v_mfma_f32_16x16x32_bf16 v[88:91], v[88:91], v[28:31], v[96:99]
	v_fmac_f32_e32 v130, v128, v108
	s_waitcnt lgkmcnt(0)
	v_mfma_f32_16x16x32_bf16 v[28:31], v[92:95], v[28:31], v[104:107]
	ds_read_b64_tr_b16 v[94:95], v193 offset:11520
	ds_read_b64_tr_b16 v[92:93], v193 offset:9216
	ds_read_b64_tr_b16 v[96:97], v193 offset:9248
	ds_read_b64_tr_b16 v[98:99], v193 offset:11552
	s_waitcnt lgkmcnt(2)
	v_mfma_f32_16x16x32_bf16 v[68:71], v[92:95], v[32:35], v[68:71]
	ds_read_b64_tr_b16 v[92:93], v193 offset:9280
	ds_read_b64_tr_b16 v[94:95], v193 offset:11584
	s_waitcnt lgkmcnt(0)
	v_mfma_f32_16x16x32_bf16 v[88:91], v[92:95], v[32:35], v[88:91]
	ds_read_b64_tr_b16 v[92:93], v193 offset:9312
	ds_read_b64_tr_b16 v[94:95], v193 offset:11616
	v_mfma_f32_16x16x32_bf16 v[76:79], v[96:99], v[32:35], v[76:79]
	s_waitcnt lgkmcnt(0)
	v_mfma_f32_16x16x32_bf16 v[108:111], v[92:95], v[32:35], v[28:31]

.LBB0_523:
	ds_read_b128 v[88:91], v191
	ds_read_b128 v[224:227], v191 offset:64
	ds_read_b128 v[228:231], v191 offset:2304
	ds_read_b128 v[232:235], v191 offset:2368
	ds_read_b128 v[236:239], v191 offset:4608
	ds_read_b128 v[240:243], v191 offset:4672
	ds_read_b128 v[244:247], v191 offset:6912
	ds_read_b128 v[182:185], v191 offset:6976
	v_mov_b32_e32 v130, v128
	v_mov_b32_e32 v134, v217
	s_waitcnt lgkmcnt(7)
	v_mfma_f32_16x16x32_bf16 v[32:35], v[88:91], v[4:7], v[32:35]
	s_waitcnt lgkmcnt(6)
	v_mfma_f32_16x16x32_bf16 v[32:35], v[224:227], v[8:11], v[32:35]
	s_nop 6
	s_waitcnt lgkmcnt(5)
	v_mfma_f32_16x16x32_bf16 v[28:31], v[228:231], v[4:7], v[28:31]
	s_waitcnt lgkmcnt(4)
	v_mfma_f32_16x16x32_bf16 v[28:31], v[232:235], v[8:11], v[28:31]
	s_waitcnt lgkmcnt(3)
	v_mfma_f32_16x16x32_bf16 v[76:79], v[236:239], v[4:7], v[76:79]
	s_waitcnt lgkmcnt(2)
	v_mfma_f32_16x16x32_bf16 v[76:79], v[240:243], v[8:11], v[76:79]
	s_waitcnt lgkmcnt(1)
	v_mfma_f32_16x16x32_bf16 v[68:71], v[244:247], v[4:7], v[68:71]
	s_waitcnt lgkmcnt(0)
	v_mfma_f32_16x16x32_bf16 v[68:71], v[182:185], v[8:11], v[68:71]
	v_max_f32_e32 v3, v34, v35
	v_max_f32_e32 v88, v30, v31
	s_nop 1
	v_max_f32_e32 v89, v76, v77
	v_max_f32_e32 v90, v78, v79
	s_nop 1
	v_max_f32_e32 v91, v70, v71
	v_max3_f32 v91, v68, v69, v91
	v_max3_f32 v3, v32, v33, v3
	v_max3_f32 v88, v28, v29, v88
	v_max3_f32 v89, v89, v90, v91
	v_max3_f32 v3, v3, v88, v89
	v_mov_b32_e32 v88, v3
	s_nop 1
	v_permlane32_swap_b32_e32 v3, v88
	v_max_f32_e32 v3, v3, v88
	v_mov_b32_e32 v88, v3
	s_nop 1
	v_permlane16_swap_b32_e32 v3, v88
	v_max3_f32 v132, v218, v3, v88
	v_sub_f32_e32 v3, v218, v132
	v_exp_f32_e32 v108, v3
	v_sub_f32_e32 v3, v32, v132
	v_exp_f32_e32 v32, v3
	v_sub_f32_e32 v3, v33, v132
	v_exp_f32_e32 v110, v3
	v_sub_f32_e32 v3, v34, v132
	v_exp_f32_e32 v33, v3
	v_sub_f32_e32 v3, v35, v132
	v_exp_f32_e32 v111, v3
	v_sub_f32_e32 v3, v28, v132
	v_exp_f32_e32 v34, v3
	v_sub_f32_e32 v3, v29, v132
	v_exp_f32_e32 v112, v3
	v_sub_f32_e32 v3, v30, v132
	v_exp_f32_e32 v35, v3
	v_sub_f32_e32 v3, v31, v132
	v_exp_f32_e32 v113, v3
	v_sub_f32_e32 v3, v76, v132
	v_exp_f32_e32 v76, v3
	v_sub_f32_e32 v3, v77, v132
	v_exp_f32_e32 v114, v3
	v_sub_f32_e32 v3, v78, v132
	v_exp_f32_e32 v77, v3
	v_sub_f32_e32 v3, v79, v132
	v_exp_f32_e32 v115, v3
	v_sub_f32_e32 v3, v68, v132
	v_exp_f32_e32 v68, v3
	v_sub_f32_e32 v3, v69, v132
	v_exp_f32_e32 v78, v3
	v_sub_f32_e32 v3, v70, v132
	v_exp_f32_e32 v69, v3
	v_sub_f32_e32 v3, v71, v132
	v_exp_f32_e32 v79, v3
	v_pk_add_f32 v[28:29], v[34:35], v[32:33]
	v_pk_add_f32 v[30:31], v[112:113], v[110:111]
	v_pk_add_f32 v[28:29], v[76:77], v[28:29]
	v_pk_add_f32 v[30:31], v[114:115], v[30:31]
	v_pk_add_f32 v[28:29], v[68:69], v[28:29]
	v_pk_add_f32 v[30:31], v[78:79], v[30:31]
	v_pk_mul_f32 v[90:91], v[74:75], v[108:109] op_sel_hi:[1,0]
	v_pk_add_f32 v[28:29], v[28:29], v[30:31]
	v_pk_mul_f32 v[88:89], v[72:73], v[108:109] op_sel_hi:[1,0]
	v_add_f32_e32 v131, v28, v29
	v_cvt_pk_bf16_f32 v28, v32, v110
	v_cvt_pk_bf16_f32 v29, v33, v111
	v_cvt_pk_bf16_f32 v30, v34, v112
	v_cvt_pk_bf16_f32 v31, v35, v113
	v_cvt_pk_bf16_f32 v32, v76, v114
	v_cvt_pk_bf16_f32 v33, v77, v115
	v_cvt_pk_bf16_f32 v34, v68, v78
	v_cvt_pk_bf16_f32 v35, v69, v79
	ds_read_b64_tr_b16 v[70:71], v192 offset:11520
	ds_read_b64_tr_b16 v[68:69], v192 offset:9216
	ds_read_b64_tr_b16 v[76:77], v192 offset:9248
	ds_read_b64_tr_b16 v[78:79], v192 offset:11552
	v_pk_mul_f32 v[94:95], v[82:83], v[108:109] op_sel_hi:[1,0]
	v_pk_mul_f32 v[92:93], v[80:81], v[108:109] op_sel_hi:[1,0]
	s_waitcnt lgkmcnt(2)
	v_mfma_f32_16x16x32_bf16 v[68:71], v[68:71], v[28:31], v[88:91]
	s_nop 2
	ds_read_b64_tr_b16 v[88:89], v192 offset:9280
	ds_read_b64_tr_b16 v[90:91], v192 offset:11584
	v_pk_mul_f32 v[98:99], v[86:87], v[108:109] op_sel_hi:[1,0]
	v_pk_mul_f32 v[96:97], v[84:85], v[108:109] op_sel_hi:[1,0]
	s_waitcnt lgkmcnt(2)
	v_mfma_f32_16x16x32_bf16 v[76:79], v[76:79], v[28:31], v[92:95]
	s_nop 2
	ds_read_b64_tr_b16 v[92:93], v192 offset:9312
	ds_read_b64_tr_b16 v[94:95], v192 offset:11616
	v_pk_mul_f32 v[106:107], v[102:103], v[108:109] op_sel_hi:[1,0]
	v_pk_mul_f32 v[104:105], v[100:101], v[108:109] op_sel_hi:[1,0]
	s_waitcnt lgkmcnt(2)
	v_mfma_f32_16x16x32_bf16 v[88:91], v[88:91], v[28:31], v[96:99]
	v_fmac_f32_e32 v131, v129, v108
	v_mov_b64_e32 v[110:111], v[66:67]
	v_mov_b64_e32 v[108:109], v[64:65]
	s_waitcnt lgkmcnt(0)
	v_mfma_f32_16x16x32_bf16 v[28:31], v[92:95], v[28:31], v[104:107]
	ds_read_b64_tr_b16 v[94:95], v193 offset:11520
	ds_read_b64_tr_b16 v[92:93], v193 offset:9216
	ds_read_b64_tr_b16 v[96:97], v193 offset:9248
	ds_read_b64_tr_b16 v[98:99], v193 offset:11552
	s_waitcnt lgkmcnt(2)
	v_mfma_f32_16x16x32_bf16 v[92:95], v[92:95], v[32:35], v[68:71]
	s_nop 2
	ds_read_b64_tr_b16 v[68:69], v193 offset:9280
	ds_read_b64_tr_b16 v[70:71], v193 offset:11584
	s_waitcnt lgkmcnt(0)
	v_mfma_f32_16x16x32_bf16 v[104:107], v[68:71], v[32:35], v[88:91]
	ds_read_b64_tr_b16 v[68:69], v193 offset:9312
	ds_read_b64_tr_b16 v[70:71], v193 offset:11616
	s_nop 0
	v_mov_b64_e32 v[90:91], v[62:63]
	v_mov_b64_e32 v[88:89], v[60:61]
	v_mfma_f32_16x16x32_bf16 v[96:99], v[96:99], v[32:35], v[76:79]
	s_waitcnt lgkmcnt(0)
	v_mfma_f32_16x16x32_bf16 v[112:115], v[68:71], v[32:35], v[28:31]
	v_mov_b64_e32 v[70:71], v[54:55]
	v_mov_b64_e32 v[78:79], v[58:59]
	v_mov_b64_e32 v[68:69], v[52:53]
	v_mov_b64_e32 v[76:77], v[56:57]

.LBB0_542:
	ds_read_b128 v[108:111], v191
	ds_read_b128 v[112:115], v191 offset:64
	ds_read_b128 v[224:227], v191 offset:2304
	ds_read_b128 v[228:231], v191 offset:2368
	ds_read_b128 v[232:235], v191 offset:4608
	ds_read_b128 v[236:239], v191 offset:4672
	ds_read_b128 v[240:243], v191 offset:6976
	ds_read_b128 v[244:247], v191 offset:6912
	s_waitcnt lgkmcnt(7)
	v_mfma_f32_16x16x32_bf16 v[68:71], v[108:111], v[4:7], v[68:71]
	v_mfma_f32_16x16x32_bf16 v[76:79], v[108:111], v[12:15], v[76:79]
	s_waitcnt lgkmcnt(6)
	v_mfma_f32_16x16x32_bf16 v[108:111], v[112:115], v[8:11], v[68:71]
	s_nop 4
	s_waitcnt lgkmcnt(5)
	v_mfma_f32_16x16x32_bf16 v[28:31], v[224:227], v[4:7], v[28:31]
	v_mfma_f32_16x16x32_bf16 v[68:71], v[224:227], v[12:15], v[88:91]
	s_nop 2
	s_waitcnt lgkmcnt(4)
	v_mfma_f32_16x16x32_bf16 v[28:31], v[228:231], v[8:11], v[28:31]
	v_mfma_f32_16x16x32_bf16 v[88:91], v[228:231], v[16:19], v[68:71]
	s_nop 2
	s_waitcnt lgkmcnt(3)
	v_mfma_f32_16x16x32_bf16 v[92:95], v[232:235], v[4:7], v[92:95]
	v_mfma_f32_16x16x32_bf16 v[68:71], v[232:235], v[12:15], v[104:107]
	s_nop 2
	s_waitcnt lgkmcnt(2)
	v_mfma_f32_16x16x32_bf16 v[134:137], v[236:239], v[8:11], v[92:95]
	s_nop 2
	v_mfma_f32_16x16x32_bf16 v[104:107], v[236:239], v[16:19], v[68:71]
	s_nop 2
	s_waitcnt lgkmcnt(0)
	v_mfma_f32_16x16x32_bf16 v[32:35], v[244:247], v[4:7], v[32:35]
	v_mfma_f32_16x16x32_bf16 v[68:71], v[244:247], v[12:15], v[96:99]
	v_mfma_f32_16x16x32_bf16 v[138:141], v[240:243], v[8:11], v[32:35]
	s_nop 5
	v_max_f32_e32 v3, v110, v111
	v_max_f32_e32 v32, v30, v31
	v_max_f32_e32 v33, v134, v135
	v_mfma_f32_16x16x32_bf16 v[92:95], v[240:243], v[16:19], v[68:71]
	v_max_f32_e32 v34, v136, v137
	v_max3_f32 v3, v108, v109, v3
	v_max_f32_e32 v35, v140, v141
	v_max3_f32 v35, v138, v139, v35
	v_max3_f32 v32, v28, v29, v32
	v_max3_f32 v33, v33, v34, v35
	v_max3_f32 v3, v3, v32, v33
	v_mov_b32_e32 v32, v3
	s_nop 1
	v_permlane32_swap_b32_e32 v3, v32
	v_max_f32_e32 v3, v3, v32
	v_mov_b32_e32 v32, v3
	s_nop 1
	v_permlane16_swap_b32_e32 v3, v32
	v_max3_f32 v132, v218, v3, v32
	v_sub_f32_e32 v3, v218, v132
	v_mfma_f32_16x16x32_bf16 v[76:79], v[112:115], v[16:19], v[76:79]
	v_exp_f32_e32 v112, v3
	v_sub_f32_e32 v3, v108, v132
	v_pk_mul_f32 v[96:97], v[72:73], v[112:113] op_sel_hi:[1,0]
	v_pk_mul_f32 v[72:73], v[80:81], v[112:113] op_sel_hi:[1,0]
	v_exp_f32_e32 v80, v3
	v_sub_f32_e32 v3, v109, v132
	v_pk_mul_f32 v[98:99], v[74:75], v[112:113] op_sel_hi:[1,0]
	v_pk_mul_f32 v[74:75], v[82:83], v[112:113] op_sel_hi:[1,0]
	v_exp_f32_e32 v82, v3
	v_sub_f32_e32 v3, v110, v132
	v_exp_f32_e32 v81, v3
	v_sub_f32_e32 v3, v111, v132
	v_exp_f32_e32 v83, v3
	v_sub_f32_e32 v3, v28, v132
	v_exp_f32_e32 v28, v3
	v_sub_f32_e32 v3, v29, v132
	v_pk_mul_f32 v[68:69], v[84:85], v[112:113] op_sel_hi:[1,0]
	v_exp_f32_e32 v84, v3
	v_sub_f32_e32 v3, v30, v132
	v_exp_f32_e32 v29, v3
	v_sub_f32_e32 v3, v31, v132
	v_exp_f32_e32 v85, v3
	v_sub_f32_e32 v3, v134, v132
	v_exp_f32_e32 v30, v3
	v_sub_f32_e32 v3, v135, v132
	v_pk_mul_f32 v[70:71], v[86:87], v[112:113] op_sel_hi:[1,0]
	v_exp_f32_e32 v86, v3
	v_sub_f32_e32 v3, v136, v132
	v_exp_f32_e32 v31, v3
	v_sub_f32_e32 v3, v137, v132
	v_exp_f32_e32 v87, v3
	v_sub_f32_e32 v3, v138, v132
	v_pk_mul_f32 v[32:33], v[100:101], v[112:113] op_sel_hi:[1,0]
	v_exp_f32_e32 v100, v3
	v_sub_f32_e32 v3, v139, v132
	v_pk_mul_f32 v[34:35], v[102:103], v[112:113] op_sel_hi:[1,0]
	v_exp_f32_e32 v102, v3
	v_sub_f32_e32 v3, v140, v132
	v_exp_f32_e32 v101, v3
	v_sub_f32_e32 v3, v141, v132
	v_exp_f32_e32 v103, v3
	v_pk_add_f32 v[108:109], v[80:81], 0 op_sel_hi:[1,0]
	v_pk_add_f32 v[110:111], v[84:85], v[82:83]
	v_cvt_pk_bf16_f32 v80, v80, v82
	v_cvt_pk_bf16_f32 v81, v81, v83
	v_cvt_pk_bf16_f32 v82, v28, v84
	v_cvt_pk_bf16_f32 v83, v29, v85
	v_max_f32_e32 v3, v78, v79
	v_pk_add_f32 v[108:109], v[28:29], v[108:109]
	v_pk_add_f32 v[110:111], v[86:87], v[110:111]
	v_cvt_pk_bf16_f32 v28, v30, v86
	v_max_f32_e32 v84, v90, v91
	v_pk_add_f32 v[108:109], v[30:31], v[108:109]
	v_cvt_pk_bf16_f32 v29, v31, v87
	v_max_f32_e32 v85, v104, v105
	v_pk_add_f32 v[108:109], v[100:101], v[108:109]
	v_cvt_pk_bf16_f32 v30, v100, v102
	v_max_f32_e32 v86, v106, v107
	v_max_f32_e32 v87, v94, v95
	v_max3_f32 v87, v92, v93, v87
	v_max3_f32 v3, v76, v77, v3
	v_max3_f32 v84, v88, v89, v84
	v_max3_f32 v85, v85, v86, v87
	v_max3_f32 v3, v3, v84, v85
	v_mov_b32_e32 v84, v3
	s_nop 1
	v_permlane32_swap_b32_e32 v3, v84
	v_max_f32_e32 v3, v3, v84
	v_mov_b32_e32 v84, v3
	s_nop 1
	v_permlane16_swap_b32_e32 v3, v84
	v_max3_f32 v134, v217, v3, v84
	v_pk_add_f32 v[110:111], v[102:103], v[110:111]
	v_sub_f32_e32 v3, v217, v134
	v_pk_add_f32 v[108:109], v[108:109], v[110:111]
	v_exp_f32_e32 v110, v3
	v_sub_f32_e32 v3, v76, v134
	v_cvt_pk_bf16_f32 v31, v101, v103
	v_pk_mul_f32 v[84:85], v[52:53], v[110:111] op_sel_hi:[1,0]
	v_exp_f32_e32 v52, v3
	v_sub_f32_e32 v3, v77, v134
	v_exp_f32_e32 v53, v3
	v_sub_f32_e32 v3, v78, v134
	v_pk_mul_f32 v[86:87], v[54:55], v[110:111] op_sel_hi:[1,0]
	v_exp_f32_e32 v54, v3
	v_sub_f32_e32 v3, v79, v134
	v_exp_f32_e32 v55, v3
	v_sub_f32_e32 v3, v88, v134
	v_pk_mul_f32 v[102:103], v[58:59], v[110:111] op_sel_hi:[1,0]
	v_pk_mul_f32 v[58:59], v[66:67], v[110:111] op_sel_hi:[1,0]
	v_exp_f32_e32 v66, v3
	v_sub_f32_e32 v3, v89, v134
	v_exp_f32_e32 v67, v3
	v_sub_f32_e32 v3, v90, v134
	v_exp_f32_e32 v76, v3
	v_sub_f32_e32 v3, v91, v134
	v_exp_f32_e32 v77, v3
	v_sub_f32_e32 v3, v104, v134
	v_exp_f32_e32 v78, v3
	v_sub_f32_e32 v3, v105, v134
	v_exp_f32_e32 v79, v3
	v_sub_f32_e32 v3, v106, v134
	v_exp_f32_e32 v88, v3
	v_sub_f32_e32 v3, v107, v134
	v_exp_f32_e32 v89, v3
	v_sub_f32_e32 v3, v92, v134
	v_exp_f32_e32 v90, v3
	v_sub_f32_e32 v3, v93, v134
	v_exp_f32_e32 v91, v3
	v_sub_f32_e32 v3, v94, v134
	v_exp_f32_e32 v92, v3
	v_sub_f32_e32 v3, v95, v134
	v_exp_f32_e32 v93, v3
	v_pk_mul_f32 v[100:101], v[56:57], v[110:111] op_sel_hi:[1,0]
	v_pk_mul_f32 v[56:57], v[64:65], v[110:111] op_sel_hi:[1,0]
	v_pk_add_f32 v[64:65], v[66:67], v[52:53]
	v_pk_add_f32 v[94:95], v[76:77], v[54:55]
	v_pk_add_f32 v[64:65], v[78:79], v[64:65]
	v_pk_add_f32 v[94:95], v[88:89], v[94:95]
	v_pk_add_f32 v[64:65], v[90:91], v[64:65]
	v_pk_add_f32 v[94:95], v[92:93], v[94:95]
	v_pk_add_f32 v[64:65], v[64:65], v[64:65] op_sel:[0,1] op_sel_hi:[1,0]
	v_pk_add_f32 v[94:95], v[94:95], v[94:95] op_sel:[0,1] op_sel_hi:[1,0]
	v_mov_b32_e32 v65, v108
	v_mov_b32_e32 v95, v109
	v_pk_mul_f32 v[62:63], v[62:63], v[110:111] op_sel_hi:[1,0]
	v_pk_mul_f32 v[60:61], v[60:61], v[110:111] op_sel_hi:[1,0]
	v_mov_b32_e32 v111, v112
	v_pk_add_f32 v[64:65], v[64:65], v[94:95]
	s_nop 0
	v_pk_fma_f32 v[130:131], v[128:129], v[110:111], v[64:65]
	v_cvt_pk_bf16_f32 v64, v52, v53
	v_cvt_pk_bf16_f32 v65, v54, v55
	v_cvt_pk_bf16_f32 v66, v66, v67
	v_cvt_pk_bf16_f32 v67, v76, v77
	v_cvt_pk_bf16_f32 v52, v78, v79
	v_cvt_pk_bf16_f32 v53, v88, v89
	v_cvt_pk_bf16_f32 v54, v90, v91
	v_cvt_pk_bf16_f32 v55, v92, v93
	ds_read_b64_tr_b16 v[78:79], v192 offset:11520
	ds_read_b64_tr_b16 v[76:77], v192 offset:9216
	ds_read_b64_tr_b16 v[88:89], v192 offset:9248
	ds_read_b64_tr_b16 v[90:91], v192 offset:11552
	s_waitcnt lgkmcnt(2)
	v_mfma_f32_16x16x32_bf16 v[92:95], v[76:79], v[80:83], v[96:99]
	v_mfma_f32_16x16x32_bf16 v[76:79], v[76:79], v[64:67], v[84:87]
	s_waitcnt lgkmcnt(0)
	v_mfma_f32_16x16x32_bf16 v[72:75], v[88:91], v[80:83], v[72:75]
	v_mfma_f32_16x16x32_bf16 v[84:87], v[88:91], v[64:67], v[100:103]
	ds_read_b64_tr_b16 v[88:89], v192 offset:9280
	ds_read_b64_tr_b16 v[90:91], v192 offset:11584
	s_waitcnt lgkmcnt(0)
	v_mfma_f32_16x16x32_bf16 v[100:103], v[88:91], v[80:83], v[68:71]
	s_nop 2
	ds_read_b64_tr_b16 v[68:69], v192 offset:9312
	ds_read_b64_tr_b16 v[70:71], v192 offset:11616
	v_mfma_f32_16x16x32_bf16 v[60:63], v[88:91], v[64:67], v[60:63]
	s_waitcnt lgkmcnt(0)
	v_mfma_f32_16x16x32_bf16 v[32:35], v[68:71], v[80:83], v[32:35]
	v_mfma_f32_16x16x32_bf16 v[56:59], v[68:71], v[64:67], v[56:59]
	ds_read_b64_tr_b16 v[66:67], v193 offset:11520
	ds_read_b64_tr_b16 v[64:65], v193 offset:9216
	ds_read_b64_tr_b16 v[80:81], v193 offset:9248
	ds_read_b64_tr_b16 v[82:83], v193 offset:11552
	s_waitcnt lgkmcnt(2)
	v_mfma_f32_16x16x32_bf16 v[92:95], v[64:67], v[28:31], v[92:95]
	v_mfma_f32_16x16x32_bf16 v[68:71], v[64:67], v[52:55], v[76:79]
	ds_read_b64_tr_b16 v[64:65], v193 offset:9280
	ds_read_b64_tr_b16 v[66:67], v193 offset:11584
	s_waitcnt lgkmcnt(0)
	v_mfma_f32_16x16x32_bf16 v[88:91], v[64:67], v[52:55], v[60:63]
	s_nop 2
	ds_read_b64_tr_b16 v[60:61], v193 offset:9312
	ds_read_b64_tr_b16 v[62:63], v193 offset:11616
	v_mfma_f32_16x16x32_bf16 v[96:99], v[80:83], v[28:31], v[72:75]
	v_mfma_f32_16x16x32_bf16 v[76:79], v[80:83], v[52:55], v[84:87]
	v_mfma_f32_16x16x32_bf16 v[104:107], v[64:67], v[28:31], v[100:103]
	s_waitcnt lgkmcnt(0)
	v_mfma_f32_16x16x32_bf16 v[112:115], v[60:63], v[28:31], v[32:35]
	v_mfma_f32_16x16x32_bf16 v[108:111], v[60:63], v[52:55], v[56:59]

.LBB0_554:
	ds_read_b128 v[60:63], v191 offset:18432
	ds_read_b128 v[224:227], v191 offset:18496
	ds_read_b128 v[228:231], v191 offset:20736
	ds_read_b128 v[232:235], v191 offset:20800
	ds_read_b128 v[236:239], v191 offset:23040
	ds_read_b128 v[240:243], v191 offset:23104
	ds_read_b128 v[244:247], v191 offset:25344
	ds_read_b128 v[182:185], v191 offset:25408
	v_mov_b32_e32 v129, v131
	s_waitcnt lgkmcnt(7)
	v_mfma_f32_16x16x32_bf16 v[24:27], v[60:63], v[12:15], v[24:27]
	s_waitcnt lgkmcnt(6)
	v_mfma_f32_16x16x32_bf16 v[24:27], v[224:227], v[16:19], v[24:27]
	s_nop 6
	s_waitcnt lgkmcnt(5)
	v_mfma_f32_16x16x32_bf16 v[20:23], v[228:231], v[12:15], v[20:23]
	s_waitcnt lgkmcnt(4)
	v_mfma_f32_16x16x32_bf16 v[20:23], v[232:235], v[16:19], v[20:23]
	s_waitcnt lgkmcnt(3)
	v_mfma_f32_16x16x32_bf16 v[56:59], v[236:239], v[12:15], v[56:59]
	s_waitcnt lgkmcnt(2)
	v_mfma_f32_16x16x32_bf16 v[56:59], v[240:243], v[16:19], v[56:59]
	s_waitcnt lgkmcnt(1)
	v_mfma_f32_16x16x32_bf16 v[52:55], v[244:247], v[12:15], v[52:55]
	s_waitcnt lgkmcnt(0)
	v_mfma_f32_16x16x32_bf16 v[52:55], v[182:185], v[16:19], v[52:55]
	v_max_f32_e32 v3, v26, v27
	v_max_f32_e32 v60, v22, v23
	s_nop 1
	v_max_f32_e32 v61, v56, v57
	v_max_f32_e32 v62, v58, v59
	s_nop 1
	v_max_f32_e32 v63, v54, v55
	v_max3_f32 v63, v52, v53, v63
	v_max3_f32 v3, v24, v25, v3
	v_max3_f32 v60, v20, v21, v60
	v_max3_f32 v61, v61, v62, v63
	v_max3_f32 v3, v3, v60, v61
	v_mov_b32_e32 v60, v3
	s_nop 1
	v_permlane32_swap_b32_e32 v3, v60
	v_max_f32_e32 v3, v3, v60
	v_mov_b32_e32 v60, v3
	s_nop 1
	v_permlane16_swap_b32_e32 v3, v60
	v_max3_f32 v3, v134, v3, v60
	v_sub_f32_e32 v25, v25, v3
	v_exp_f32_e32 v86, v25
	v_sub_f32_e32 v25, v26, v3
	v_sub_f32_e32 v26, v27, v3
	v_sub_f32_e32 v20, v20, v3
	v_exp_f32_e32 v87, v26
	v_exp_f32_e32 v26, v20
	v_sub_f32_e32 v20, v21, v3
	v_exp_f32_e32 v100, v20
	v_sub_f32_e32 v20, v22, v3
	v_exp_f32_e32 v27, v20
	v_sub_f32_e32 v20, v23, v3
	v_exp_f32_e32 v101, v20
	v_sub_f32_e32 v20, v56, v3
	v_exp_f32_e32 v56, v20
	v_sub_f32_e32 v20, v57, v3
	v_exp_f32_e32 v102, v20
	v_sub_f32_e32 v20, v58, v3
	v_exp_f32_e32 v57, v20
	v_sub_f32_e32 v20, v59, v3
	v_sub_f32_e32 v24, v24, v3
	v_exp_f32_e32 v103, v20
	v_sub_f32_e32 v20, v52, v3
	v_exp_f32_e32 v24, v24
	v_exp_f32_e32 v25, v25
	v_exp_f32_e32 v52, v20
	v_sub_f32_e32 v20, v53, v3
	v_exp_f32_e32 v58, v20
	v_sub_f32_e32 v20, v54, v3
	v_exp_f32_e32 v53, v20
	v_sub_f32_e32 v20, v55, v3
	v_exp_f32_e32 v59, v20
	v_pk_add_f32 v[20:21], v[26:27], v[24:25]
	v_pk_add_f32 v[22:23], v[100:101], v[86:87]
	v_pk_add_f32 v[20:21], v[56:57], v[20:21]
	v_pk_add_f32 v[22:23], v[102:103], v[22:23]
	v_pk_add_f32 v[20:21], v[52:53], v[20:21]
	v_pk_add_f32 v[22:23], v[58:59], v[22:23]
	v_sub_f32_e32 v60, v134, v3
	v_pk_add_f32 v[20:21], v[20:21], v[22:23]
	v_exp_f32_e32 v84, v60
	v_add_f32_e32 v128, v20, v21
	v_cvt_pk_bf16_f32 v20, v24, v86
	v_cvt_pk_bf16_f32 v21, v25, v87
	v_cvt_pk_bf16_f32 v22, v26, v100
	v_cvt_pk_bf16_f32 v23, v27, v101
	v_cvt_pk_bf16_f32 v24, v56, v102
	v_cvt_pk_bf16_f32 v25, v57, v103
	v_cvt_pk_bf16_f32 v26, v52, v58
	v_cvt_pk_bf16_f32 v27, v53, v59
	ds_read_b64_tr_b16 v[54:55], v192 offset:29952
	ds_read_b64_tr_b16 v[52:53], v192 offset:27648
	ds_read_b64_tr_b16 v[56:57], v192 offset:27680
	ds_read_b64_tr_b16 v[58:59], v192 offset:29984
	v_pk_mul_f32 v[62:63], v[70:71], v[84:85] op_sel_hi:[1,0]
	v_pk_mul_f32 v[60:61], v[68:69], v[84:85] op_sel_hi:[1,0]
	v_pk_mul_f32 v[66:67], v[78:79], v[84:85] op_sel_hi:[1,0]
	v_pk_mul_f32 v[64:65], v[76:77], v[84:85] op_sel_hi:[1,0]
	s_waitcnt lgkmcnt(2)
	v_mfma_f32_16x16x32_bf16 v[52:55], v[52:55], v[20:23], v[60:63]
	s_nop 2
	ds_read_b64_tr_b16 v[60:61], v192 offset:27712
	ds_read_b64_tr_b16 v[62:63], v192 offset:30016
	v_pk_mul_f32 v[74:75], v[90:91], v[84:85] op_sel_hi:[1,0]
	v_pk_mul_f32 v[72:73], v[88:89], v[84:85] op_sel_hi:[1,0]
	s_waitcnt lgkmcnt(2)
	v_mfma_f32_16x16x32_bf16 v[56:59], v[56:59], v[20:23], v[64:67]
	s_nop 2
	ds_read_b64_tr_b16 v[64:65], v192 offset:27744
	ds_read_b64_tr_b16 v[66:67], v192 offset:30048
	v_pk_mul_f32 v[82:83], v[110:111], v[84:85] op_sel_hi:[1,0]
	v_pk_mul_f32 v[80:81], v[108:109], v[84:85] op_sel_hi:[1,0]
	s_waitcnt lgkmcnt(2)
	v_mfma_f32_16x16x32_bf16 v[60:63], v[60:63], v[20:23], v[72:75]
	v_fmac_f32_e32 v128, v130, v84
	s_waitcnt lgkmcnt(0)
	v_mfma_f32_16x16x32_bf16 v[20:23], v[64:67], v[20:23], v[80:83]
	ds_read_b64_tr_b16 v[66:67], v193 offset:29952
	ds_read_b64_tr_b16 v[64:65], v193 offset:27648
	ds_read_b64_tr_b16 v[72:73], v193 offset:27680
	ds_read_b64_tr_b16 v[74:75], v193 offset:29984
	s_waitcnt lgkmcnt(2)
	v_mfma_f32_16x16x32_bf16 v[52:55], v[64:67], v[24:27], v[52:55]
	ds_read_b64_tr_b16 v[64:65], v193 offset:27712
	ds_read_b64_tr_b16 v[66:67], v193 offset:30016
	s_waitcnt lgkmcnt(0)
	v_mfma_f32_16x16x32_bf16 v[60:63], v[64:67], v[24:27], v[60:63]
	ds_read_b64_tr_b16 v[64:65], v193 offset:27744
	ds_read_b64_tr_b16 v[66:67], v193 offset:30048
	v_mfma_f32_16x16x32_bf16 v[56:59], v[72:75], v[24:27], v[56:59]
	s_waitcnt lgkmcnt(0)
	v_mfma_f32_16x16x32_bf16 v[84:87], v[64:67], v[24:27], v[20:23]

.LBB0_565:
	ds_read_b128 v[60:63], v191 offset:18432
	ds_read_b128 v[224:227], v191 offset:18496
	ds_read_b128 v[228:231], v191 offset:20736
	ds_read_b128 v[232:235], v191 offset:20800
	ds_read_b128 v[236:239], v191 offset:23040
	ds_read_b128 v[240:243], v191 offset:23104
	ds_read_b128 v[244:247], v191 offset:25344
	ds_read_b128 v[182:185], v191 offset:25408
	v_mov_b32_e32 v128, v130
	s_waitcnt lgkmcnt(7)
	v_mfma_f32_16x16x32_bf16 v[24:27], v[60:63], v[4:7], v[24:27]
	s_waitcnt lgkmcnt(6)
	v_mfma_f32_16x16x32_bf16 v[24:27], v[224:227], v[8:11], v[24:27]
	s_nop 6
	s_waitcnt lgkmcnt(5)
	v_mfma_f32_16x16x32_bf16 v[20:23], v[228:231], v[4:7], v[20:23]
	s_waitcnt lgkmcnt(4)
	v_mfma_f32_16x16x32_bf16 v[20:23], v[232:235], v[8:11], v[20:23]
	s_waitcnt lgkmcnt(3)
	v_mfma_f32_16x16x32_bf16 v[56:59], v[236:239], v[4:7], v[56:59]
	s_waitcnt lgkmcnt(2)
	v_mfma_f32_16x16x32_bf16 v[56:59], v[240:243], v[8:11], v[56:59]
	s_waitcnt lgkmcnt(1)
	v_mfma_f32_16x16x32_bf16 v[52:55], v[244:247], v[4:7], v[52:55]
	s_waitcnt lgkmcnt(0)
	v_mfma_f32_16x16x32_bf16 v[52:55], v[182:185], v[8:11], v[52:55]
	v_max_f32_e32 v3, v26, v27
	v_max_f32_e32 v60, v22, v23
	s_nop 1
	v_max_f32_e32 v61, v56, v57
	v_max_f32_e32 v62, v58, v59
	s_nop 1
	v_max_f32_e32 v63, v54, v55
	v_max3_f32 v63, v52, v53, v63
	v_max3_f32 v3, v24, v25, v3
	v_max3_f32 v60, v20, v21, v60
	v_max3_f32 v61, v61, v62, v63
	v_max3_f32 v3, v3, v60, v61
	v_mov_b32_e32 v60, v3
	s_nop 1
	v_permlane32_swap_b32_e32 v3, v60
	v_max_f32_e32 v3, v3, v60
	v_mov_b32_e32 v60, v3
	s_nop 1
	v_permlane16_swap_b32_e32 v3, v60
	v_max3_f32 v217, v132, v3, v60
	v_sub_f32_e32 v3, v132, v217
	v_exp_f32_e32 v84, v3
	v_sub_f32_e32 v3, v24, v217
	v_exp_f32_e32 v24, v3
	v_sub_f32_e32 v3, v25, v217
	v_exp_f32_e32 v86, v3
	v_sub_f32_e32 v3, v26, v217
	v_exp_f32_e32 v25, v3
	v_sub_f32_e32 v3, v27, v217
	v_exp_f32_e32 v87, v3
	v_sub_f32_e32 v3, v20, v217
	v_exp_f32_e32 v26, v3
	v_sub_f32_e32 v3, v21, v217
	v_exp_f32_e32 v100, v3
	v_sub_f32_e32 v3, v22, v217
	v_exp_f32_e32 v27, v3
	v_sub_f32_e32 v3, v23, v217
	v_exp_f32_e32 v101, v3
	v_sub_f32_e32 v3, v56, v217
	v_exp_f32_e32 v56, v3
	v_sub_f32_e32 v3, v57, v217
	v_exp_f32_e32 v102, v3
	v_sub_f32_e32 v3, v58, v217
	v_exp_f32_e32 v57, v3
	v_sub_f32_e32 v3, v59, v217
	v_exp_f32_e32 v103, v3
	v_sub_f32_e32 v3, v52, v217
	v_exp_f32_e32 v52, v3
	v_sub_f32_e32 v3, v53, v217
	v_exp_f32_e32 v58, v3
	v_sub_f32_e32 v3, v54, v217
	v_exp_f32_e32 v53, v3
	v_sub_f32_e32 v3, v55, v217
	v_exp_f32_e32 v59, v3
	v_pk_add_f32 v[20:21], v[26:27], v[24:25]
	v_pk_add_f32 v[22:23], v[100:101], v[86:87]
	v_pk_add_f32 v[20:21], v[56:57], v[20:21]
	v_pk_add_f32 v[22:23], v[102:103], v[22:23]
	v_pk_add_f32 v[20:21], v[52:53], v[20:21]
	v_pk_add_f32 v[22:23], v[58:59], v[22:23]
	v_pk_mul_f32 v[62:63], v[94:95], v[84:85] op_sel_hi:[1,0]
	v_pk_add_f32 v[20:21], v[20:21], v[22:23]
	v_pk_mul_f32 v[60:61], v[92:93], v[84:85] op_sel_hi:[1,0]
	v_add_f32_e32 v129, v20, v21
	v_cvt_pk_bf16_f32 v20, v24, v86
	v_cvt_pk_bf16_f32 v21, v25, v87
	v_cvt_pk_bf16_f32 v22, v26, v100
	v_cvt_pk_bf16_f32 v23, v27, v101
	v_cvt_pk_bf16_f32 v24, v56, v102
	v_cvt_pk_bf16_f32 v25, v57, v103
	v_cvt_pk_bf16_f32 v26, v52, v58
	v_cvt_pk_bf16_f32 v27, v53, v59
	ds_read_b64_tr_b16 v[54:55], v192 offset:29952
	ds_read_b64_tr_b16 v[52:53], v192 offset:27648
	ds_read_b64_tr_b16 v[56:57], v192 offset:27680
	ds_read_b64_tr_b16 v[58:59], v192 offset:29984
	v_pk_mul_f32 v[66:67], v[98:99], v[84:85] op_sel_hi:[1,0]
	v_pk_mul_f32 v[64:65], v[96:97], v[84:85] op_sel_hi:[1,0]
	s_waitcnt lgkmcnt(2)
	v_mfma_f32_16x16x32_bf16 v[52:55], v[52:55], v[20:23], v[60:63]
	s_nop 2
	ds_read_b64_tr_b16 v[60:61], v192 offset:27712
	ds_read_b64_tr_b16 v[62:63], v192 offset:30016
	v_pk_mul_f32 v[74:75], v[106:107], v[84:85] op_sel_hi:[1,0]
	v_pk_mul_f32 v[72:73], v[104:105], v[84:85] op_sel_hi:[1,0]
	s_waitcnt lgkmcnt(2)
	v_mfma_f32_16x16x32_bf16 v[56:59], v[56:59], v[20:23], v[64:67]
	s_nop 2
	ds_read_b64_tr_b16 v[64:65], v192 offset:27744
	ds_read_b64_tr_b16 v[66:67], v192 offset:30048
	v_pk_mul_f32 v[82:83], v[114:115], v[84:85] op_sel_hi:[1,0]
	v_pk_mul_f32 v[80:81], v[112:113], v[84:85] op_sel_hi:[1,0]
	s_waitcnt lgkmcnt(2)
	v_mfma_f32_16x16x32_bf16 v[60:63], v[60:63], v[20:23], v[72:75]
	v_fmac_f32_e32 v129, v131, v84
	v_mov_b64_e32 v[84:85], v[108:109]
	v_mov_b32_e32 v3, v134
	s_waitcnt lgkmcnt(0)
	v_mfma_f32_16x16x32_bf16 v[20:23], v[64:67], v[20:23], v[80:83]
	ds_read_b64_tr_b16 v[66:67], v193 offset:29952
	ds_read_b64_tr_b16 v[64:65], v193 offset:27648
	ds_read_b64_tr_b16 v[72:73], v193 offset:27680
	ds_read_b64_tr_b16 v[74:75], v193 offset:29984
	v_mov_b64_e32 v[86:87], v[110:111]
	s_waitcnt lgkmcnt(2)
	v_mfma_f32_16x16x32_bf16 v[64:67], v[64:67], v[24:27], v[52:55]
	s_nop 2
	ds_read_b64_tr_b16 v[52:53], v193 offset:27712
	ds_read_b64_tr_b16 v[54:55], v193 offset:30016
	s_waitcnt lgkmcnt(0)
	v_mfma_f32_16x16x32_bf16 v[80:83], v[52:55], v[24:27], v[60:63]
	ds_read_b64_tr_b16 v[52:53], v193 offset:27744
	ds_read_b64_tr_b16 v[54:55], v193 offset:30048
	s_nop 0
	v_mov_b64_e32 v[60:61], v[88:89]
	v_mov_b64_e32 v[62:63], v[90:91]
	v_mfma_f32_16x16x32_bf16 v[72:75], v[72:75], v[24:27], v[56:59]
	s_waitcnt lgkmcnt(0)
	v_mfma_f32_16x16x32_bf16 v[100:103], v[52:55], v[24:27], v[20:23]
	v_mov_b64_e32 v[52:53], v[68:69]
	v_mov_b64_e32 v[56:57], v[76:77]
	v_mov_b64_e32 v[54:55], v[70:71]
	v_mov_b64_e32 v[58:59], v[78:79]

.LBB0_584:
	ds_read_b128 v[80:83], v191 offset:18432
	ds_read_b128 v[84:87], v191 offset:18496
	ds_read_b128 v[224:227], v191 offset:20736
	ds_read_b128 v[228:231], v191 offset:20800
	ds_read_b128 v[232:235], v191 offset:23040
	ds_read_b128 v[236:239], v191 offset:23104
	ds_read_b128 v[240:243], v191 offset:25344
	ds_read_b128 v[244:247], v191 offset:25408
	s_waitcnt lgkmcnt(7)
	v_mfma_f32_16x16x32_bf16 v[52:55], v[80:83], v[4:7], v[52:55]
	v_mfma_f32_16x16x32_bf16 v[80:83], v[80:83], v[12:15], v[60:63]
	s_waitcnt lgkmcnt(6)
	v_mfma_f32_16x16x32_bf16 v[60:63], v[84:87], v[8:11], v[52:55]
	s_nop 4
	s_waitcnt lgkmcnt(5)
	v_mfma_f32_16x16x32_bf16 v[20:23], v[224:227], v[4:7], v[20:23]
	v_mfma_f32_16x16x32_bf16 v[52:55], v[224:227], v[12:15], v[64:67]
	s_nop 2
	v_mfma_f32_16x16x32_bf16 v[80:83], v[84:87], v[16:19], v[80:83]
	s_waitcnt lgkmcnt(4)
	v_mfma_f32_16x16x32_bf16 v[84:87], v[228:231], v[16:19], v[52:55]
	s_nop 2
	v_mfma_f32_16x16x32_bf16 v[20:23], v[228:231], v[8:11], v[20:23]
	s_waitcnt lgkmcnt(3)
	v_mfma_f32_16x16x32_bf16 v[56:59], v[232:235], v[4:7], v[56:59]
	v_mfma_f32_16x16x32_bf16 v[52:55], v[232:235], v[12:15], v[100:103]
	s_waitcnt lgkmcnt(2)
	v_mfma_f32_16x16x32_bf16 v[100:103], v[236:239], v[16:19], v[52:55]
	v_mfma_f32_16x16x32_bf16 v[146:149], v[236:239], v[8:11], v[56:59]
	s_nop 4
	s_waitcnt lgkmcnt(1)
	v_mfma_f32_16x16x32_bf16 v[24:27], v[240:243], v[4:7], v[24:27]
	v_mfma_f32_16x16x32_bf16 v[52:55], v[240:243], v[12:15], v[72:75]
	s_waitcnt lgkmcnt(0)
	v_mfma_f32_16x16x32_bf16 v[154:157], v[244:247], v[8:11], v[24:27]
	s_nop 4
	v_max_f32_e32 v3, v62, v63
	v_max_f32_e32 v24, v22, v23
	v_max_f32_e32 v25, v146, v147
	v_mfma_f32_16x16x32_bf16 v[56:59], v[244:247], v[16:19], v[52:55]
	v_max_f32_e32 v26, v148, v149
	v_max3_f32 v3, v60, v61, v3
	v_max_f32_e32 v27, v156, v157
	v_max3_f32 v27, v154, v155, v27
	v_max3_f32 v24, v20, v21, v24
	v_max3_f32 v25, v25, v26, v27
	v_max3_f32 v3, v3, v24, v25
	v_mov_b32_e32 v24, v3
	s_nop 1
	v_permlane32_swap_b32_e32 v3, v24
	v_max_f32_e32 v3, v3, v24
	v_mov_b32_e32 v24, v3
	s_nop 1
	v_permlane16_swap_b32_e32 v3, v24
	v_max3_f32 v217, v132, v3, v24
	v_sub_f32_e32 v3, v132, v217
	v_exp_f32_e32 v128, v3
	v_sub_f32_e32 v3, v60, v217
	v_pk_mul_f32 v[52:53], v[104:105], v[128:129] op_sel_hi:[1,0]
	v_exp_f32_e32 v105, v3
	v_sub_f32_e32 v3, v61, v217
	v_pk_mul_f32 v[54:55], v[106:107], v[128:129] op_sel_hi:[1,0]
	v_exp_f32_e32 v107, v3
	v_sub_f32_e32 v3, v62, v217
	v_pk_mul_f32 v[24:25], v[112:113], v[128:129] op_sel_hi:[1,0]
	v_exp_f32_e32 v113, v3
	v_sub_f32_e32 v3, v63, v217
	v_pk_mul_f32 v[26:27], v[114:115], v[128:129] op_sel_hi:[1,0]
	v_exp_f32_e32 v115, v3
	v_sub_f32_e32 v3, v20, v217
	v_exp_f32_e32 v133, v3
	v_sub_f32_e32 v3, v21, v217
	v_exp_f32_e32 v135, v3
	v_sub_f32_e32 v3, v22, v217
	v_exp_f32_e32 v139, v3
	v_sub_f32_e32 v3, v23, v217
	v_exp_f32_e32 v143, v3
	v_sub_f32_e32 v3, v146, v217
	v_exp_f32_e32 v137, v3
	v_sub_f32_e32 v3, v147, v217
	v_exp_f32_e32 v141, v3
	v_sub_f32_e32 v3, v148, v217
	v_exp_f32_e32 v147, v3
	v_sub_f32_e32 v3, v149, v217
	v_exp_f32_e32 v149, v3
	v_sub_f32_e32 v3, v154, v217
	v_exp_f32_e32 v151, v3
	v_sub_f32_e32 v3, v155, v217
	v_exp_f32_e32 v153, v3
	v_sub_f32_e32 v3, v156, v217
	v_exp_f32_e32 v155, v3
	v_sub_f32_e32 v3, v157, v217
	v_pk_mul_f32 v[72:73], v[92:93], v[128:129] op_sel_hi:[1,0]
	v_exp_f32_e32 v157, v3
	v_max_f32_e32 v3, v82, v83
	v_pk_mul_f32 v[74:75], v[94:95], v[128:129] op_sel_hi:[1,0]
	v_max_f32_e32 v92, v86, v87
	v_max_f32_e32 v93, v100, v101
	v_pk_mul_f32 v[64:65], v[96:97], v[128:129] op_sel_hi:[1,0]
	v_max_f32_e32 v94, v102, v103
	v_max_f32_e32 v95, v58, v59
	v_max3_f32 v95, v56, v57, v95
	v_max3_f32 v3, v80, v81, v3
	v_max3_f32 v92, v84, v85, v92
	v_max3_f32 v93, v93, v94, v95
	v_max3_f32 v3, v3, v92, v93
	v_mov_b32_e32 v92, v3
	s_nop 1
	v_permlane32_swap_b32_e32 v3, v92
	v_max_f32_e32 v3, v3, v92
	v_mov_b32_e32 v92, v3
	s_nop 1
	v_permlane16_swap_b32_e32 v3, v92
	v_max3_f32 v3, v134, v3, v92
	v_sub_f32_e32 v92, v134, v3
	v_exp_f32_e32 v218, v92
	v_sub_f32_e32 v56, v56, v3
	v_sub_f32_e32 v58, v58, v3
	v_exp_f32_e32 v150, v56
	v_pk_mul_f32 v[92:93], v[76:77], v[218:219] op_sel_hi:[1,0]
	v_sub_f32_e32 v76, v80, v3
	v_exp_f32_e32 v104, v76
	v_sub_f32_e32 v76, v81, v3
	v_exp_f32_e32 v106, v76
	v_sub_f32_e32 v76, v82, v3
	v_exp_f32_e32 v112, v76
	v_sub_f32_e32 v76, v83, v3
	v_exp_f32_e32 v114, v76
	v_sub_f32_e32 v76, v84, v3
	v_exp_f32_e32 v132, v76
	v_sub_f32_e32 v76, v85, v3
	v_exp_f32_e32 v134, v76
	v_sub_f32_e32 v76, v86, v3
	v_exp_f32_e32 v138, v76
	v_sub_f32_e32 v76, v87, v3
	v_exp_f32_e32 v142, v76
	v_sub_f32_e32 v76, v100, v3
	v_exp_f32_e32 v136, v76
	v_sub_f32_e32 v76, v101, v3
	v_exp_f32_e32 v140, v76
	v_sub_f32_e32 v76, v102, v3
	v_exp_f32_e32 v146, v76
	v_sub_f32_e32 v76, v103, v3
	v_exp_f32_e32 v148, v76
	v_sub_f32_e32 v56, v57, v3
	v_exp_f32_e32 v154, v58
	v_sub_f32_e32 v58, v59, v3
	v_exp_f32_e32 v152, v56
	v_exp_f32_e32 v156, v58
	v_pk_mul_f32 v[94:95], v[78:79], v[218:219] op_sel_hi:[1,0]
	v_pk_add_f32 v[76:77], v[132:133], v[104:105]
	v_pk_add_f32 v[56:57], v[134:135], v[106:107]
	v_pk_add_f32 v[78:79], v[138:139], v[112:113]
	v_pk_add_f32 v[58:59], v[142:143], v[114:115]
	v_pk_add_f32 v[76:77], v[136:137], v[76:77]
	v_pk_add_f32 v[56:57], v[140:141], v[56:57]
	v_pk_add_f32 v[78:79], v[146:147], v[78:79]
	v_pk_add_f32 v[58:59], v[148:149], v[58:59]
	v_pk_add_f32 v[76:77], v[150:151], v[76:77]
	v_pk_add_f32 v[56:57], v[152:153], v[56:57]
	v_pk_add_f32 v[78:79], v[154:155], v[78:79]
	v_pk_add_f32 v[58:59], v[156:157], v[58:59]
	v_pk_add_f32 v[56:57], v[76:77], v[56:57]
	v_pk_add_f32 v[58:59], v[78:79], v[58:59]
	v_pk_mul_f32 v[66:67], v[98:99], v[128:129] op_sel_hi:[1,0]
	v_pk_mul_f32 v[98:99], v[70:71], v[218:219] op_sel_hi:[1,0]
	v_pk_mul_f32 v[96:97], v[68:69], v[218:219] op_sel_hi:[1,0]
	v_pk_mul_f32 v[90:91], v[90:91], v[218:219] op_sel_hi:[1,0]
	v_pk_mul_f32 v[88:89], v[88:89], v[218:219] op_sel_hi:[1,0]
	v_pk_mul_f32 v[70:71], v[110:111], v[218:219] op_sel_hi:[1,0]
	v_pk_mul_f32 v[68:69], v[108:109], v[218:219] op_sel_hi:[1,0]
	v_mov_b32_e32 v219, v128
	v_pk_add_f32 v[56:57], v[56:57], v[58:59]
	v_cvt_pk_bf16_f32 v60, v105, v107
	v_cvt_pk_bf16_f32 v61, v113, v115
	v_cvt_pk_bf16_f32 v62, v133, v135
	v_cvt_pk_bf16_f32 v63, v139, v143
	v_cvt_pk_bf16_f32 v20, v137, v141
	v_cvt_pk_bf16_f32 v21, v147, v149
	v_cvt_pk_bf16_f32 v22, v151, v153
	v_cvt_pk_bf16_f32 v23, v155, v157
	s_nop 0
	v_pk_fma_f32 v[128:129], v[130:131], v[218:219], v[56:57]
	v_cvt_pk_bf16_f32 v56, v104, v106
	v_cvt_pk_bf16_f32 v57, v112, v114
	v_cvt_pk_bf16_f32 v58, v132, v134
	v_cvt_pk_bf16_f32 v59, v138, v142
	v_cvt_pk_bf16_f32 v76, v136, v140
	v_cvt_pk_bf16_f32 v77, v146, v148
	v_cvt_pk_bf16_f32 v78, v150, v152
	v_cvt_pk_bf16_f32 v79, v154, v156
	ds_read_b64_tr_b16 v[82:83], v192 offset:29952
	ds_read_b64_tr_b16 v[80:81], v192 offset:27648
	ds_read_b64_tr_b16 v[84:85], v192 offset:27680
	ds_read_b64_tr_b16 v[86:87], v192 offset:29984
	s_waitcnt lgkmcnt(2)
	v_mfma_f32_16x16x32_bf16 v[72:75], v[80:83], v[60:63], v[72:75]
	v_mfma_f32_16x16x32_bf16 v[80:83], v[80:83], v[56:59], v[96:99]
	s_waitcnt lgkmcnt(0)
	v_mfma_f32_16x16x32_bf16 v[96:99], v[84:87], v[60:63], v[64:67]
	s_nop 2
	ds_read_b64_tr_b16 v[64:65], v192 offset:27712
	ds_read_b64_tr_b16 v[66:67], v192 offset:30016
	v_mfma_f32_16x16x32_bf16 v[84:87], v[84:87], v[56:59], v[92:95]
	s_waitcnt lgkmcnt(0)
	v_mfma_f32_16x16x32_bf16 v[92:95], v[64:67], v[60:63], v[52:55]
	s_nop 2
	ds_read_b64_tr_b16 v[52:53], v192 offset:27744
	ds_read_b64_tr_b16 v[54:55], v192 offset:30048
	v_mfma_f32_16x16x32_bf16 v[88:91], v[64:67], v[56:59], v[88:91]
	s_waitcnt lgkmcnt(0)
	v_mfma_f32_16x16x32_bf16 v[24:27], v[52:55], v[60:63], v[24:27]
	v_mfma_f32_16x16x32_bf16 v[68:71], v[52:55], v[56:59], v[68:71]
	ds_read_b64_tr_b16 v[54:55], v193 offset:29952
	ds_read_b64_tr_b16 v[52:53], v193 offset:27648
	ds_read_b64_tr_b16 v[56:57], v193 offset:27680
	ds_read_b64_tr_b16 v[58:59], v193 offset:29984
	ds_read_b64_tr_b16 v[60:61], v193 offset:27712
	ds_read_b64_tr_b16 v[62:63], v193 offset:30016
	s_waitcnt lgkmcnt(4)
	v_mfma_f32_16x16x32_bf16 v[64:67], v[52:55], v[20:23], v[72:75]
	s_waitcnt lgkmcnt(2)
	v_mfma_f32_16x16x32_bf16 v[72:75], v[56:59], v[20:23], v[96:99]
	v_mfma_f32_16x16x32_bf16 v[56:59], v[56:59], v[76:79], v[84:87]
	s_nop 2
	ds_read_b64_tr_b16 v[84:85], v193 offset:27744
	ds_read_b64_tr_b16 v[86:87], v193 offset:30048
	v_mfma_f32_16x16x32_bf16 v[52:55], v[52:55], v[76:79], v[80:83]
	s_waitcnt lgkmcnt(2)
	v_mfma_f32_16x16x32_bf16 v[80:83], v[60:63], v[20:23], v[92:95]
	v_mfma_f32_16x16x32_bf16 v[60:63], v[60:63], v[76:79], v[88:91]
	s_waitcnt lgkmcnt(0)
	v_mfma_f32_16x16x32_bf16 v[100:103], v[84:87], v[20:23], v[24:27]
	v_mfma_f32_16x16x32_bf16 v[84:87], v[84:87], v[76:79], v[68:71]

.LBB0_596:
	ds_read_b128 v[88:91], v191
	ds_read_b128 v[224:227], v191 offset:64
	ds_read_b128 v[228:231], v191 offset:2304
	ds_read_b128 v[232:235], v191 offset:2368
	ds_read_b128 v[236:239], v191 offset:4608
	ds_read_b128 v[240:243], v191 offset:4672
	ds_read_b128 v[244:247], v191 offset:6912
	ds_read_b128 v[182:185], v191 offset:6976
	v_mov_b32_e32 v131, v129
	s_waitcnt lgkmcnt(7)
	v_mfma_f32_16x16x32_bf16 v[40:43], v[88:91], v[12:15], v[40:43]
	s_waitcnt lgkmcnt(6)
	v_mfma_f32_16x16x32_bf16 v[40:43], v[224:227], v[16:19], v[40:43]
	s_waitcnt lgkmcnt(5)
	v_mfma_f32_16x16x32_bf16 v[36:39], v[228:231], v[12:15], v[36:39]
	s_waitcnt lgkmcnt(4)
	v_mfma_f32_16x16x32_bf16 v[36:39], v[232:235], v[16:19], v[36:39]
	s_waitcnt lgkmcnt(3)
	v_mfma_f32_16x16x32_bf16 v[76:79], v[236:239], v[12:15], v[76:79]
	s_waitcnt lgkmcnt(2)
	v_mfma_f32_16x16x32_bf16 v[76:79], v[240:243], v[16:19], v[76:79]
	s_nop 6
	s_waitcnt lgkmcnt(1)
	v_mfma_f32_16x16x32_bf16 v[68:71], v[244:247], v[12:15], v[68:71]
	s_waitcnt lgkmcnt(0)
	v_mfma_f32_16x16x32_bf16 v[68:71], v[182:185], v[16:19], v[68:71]
	v_max_f32_e32 v88, v42, v43
	v_max_f32_e32 v89, v38, v39
	v_max_f32_e32 v90, v76, v77
	v_max_f32_e32 v91, v78, v79
	s_nop 3
	v_max_f32_e32 v92, v70, v71
	v_max3_f32 v92, v68, v69, v92
	v_max3_f32 v88, v40, v41, v88
	v_max3_f32 v89, v36, v37, v89
	v_max3_f32 v90, v90, v91, v92
	v_max3_f32 v88, v88, v89, v90
	v_mov_b32_e32 v89, v88
	s_nop 1
	v_permlane32_swap_b32_e32 v88, v89
	v_max_f32_e32 v88, v88, v89
	v_mov_b32_e32 v89, v88
	s_nop 1
	v_permlane16_swap_b32_e32 v88, v89
	v_max3_f32 v219, v3, v88, v89
	v_sub_f32_e32 v41, v41, v219
	v_exp_f32_e32 v110, v41
	v_sub_f32_e32 v41, v42, v219
	v_sub_f32_e32 v42, v43, v219
	v_sub_f32_e32 v36, v36, v219
	v_exp_f32_e32 v111, v42
	v_exp_f32_e32 v42, v36
	v_sub_f32_e32 v36, v37, v219
	v_exp_f32_e32 v112, v36
	v_sub_f32_e32 v36, v38, v219
	v_exp_f32_e32 v43, v36
	v_sub_f32_e32 v36, v39, v219
	v_exp_f32_e32 v113, v36
	v_sub_f32_e32 v36, v76, v219
	v_exp_f32_e32 v76, v36
	v_sub_f32_e32 v36, v77, v219
	v_exp_f32_e32 v114, v36
	v_sub_f32_e32 v36, v78, v219
	v_exp_f32_e32 v77, v36
	v_sub_f32_e32 v36, v79, v219
	v_sub_f32_e32 v40, v40, v219
	v_exp_f32_e32 v115, v36
	v_sub_f32_e32 v36, v68, v219
	v_exp_f32_e32 v40, v40
	v_exp_f32_e32 v41, v41
	v_exp_f32_e32 v68, v36
	v_sub_f32_e32 v36, v69, v219
	v_exp_f32_e32 v78, v36
	v_sub_f32_e32 v36, v70, v219
	v_exp_f32_e32 v69, v36
	v_sub_f32_e32 v36, v71, v219
	v_exp_f32_e32 v79, v36
	v_pk_add_f32 v[36:37], v[42:43], v[40:41]
	v_pk_add_f32 v[38:39], v[112:113], v[110:111]
	v_pk_add_f32 v[36:37], v[76:77], v[36:37]
	v_pk_add_f32 v[38:39], v[114:115], v[38:39]
	v_pk_add_f32 v[36:37], v[68:69], v[36:37]
	v_pk_add_f32 v[38:39], v[78:79], v[38:39]
	v_sub_f32_e32 v88, v3, v219
	v_pk_add_f32 v[36:37], v[36:37], v[38:39]
	v_exp_f32_e32 v108, v88
	v_add_f32_e32 v130, v36, v37
	v_cvt_pk_bf16_f32 v36, v40, v110
	v_cvt_pk_bf16_f32 v37, v41, v111
	v_cvt_pk_bf16_f32 v38, v42, v112
	v_cvt_pk_bf16_f32 v39, v43, v113
	v_cvt_pk_bf16_f32 v40, v76, v114
	v_cvt_pk_bf16_f32 v41, v77, v115
	v_cvt_pk_bf16_f32 v42, v68, v78
	v_cvt_pk_bf16_f32 v43, v69, v79
	ds_read_b64_tr_b16 v[70:71], v192 offset:11520
	ds_read_b64_tr_b16 v[68:69], v192 offset:9216
	ds_read_b64_tr_b16 v[76:77], v192 offset:9248
	ds_read_b64_tr_b16 v[78:79], v192 offset:11552
	v_pk_mul_f32 v[90:91], v[54:55], v[108:109] op_sel_hi:[1,0]
	v_pk_mul_f32 v[88:89], v[52:53], v[108:109] op_sel_hi:[1,0]
	v_pk_mul_f32 v[94:95], v[58:59], v[108:109] op_sel_hi:[1,0]
	v_pk_mul_f32 v[92:93], v[56:57], v[108:109] op_sel_hi:[1,0]
	s_waitcnt lgkmcnt(2)
	v_mfma_f32_16x16x32_bf16 v[68:71], v[68:71], v[36:39], v[88:91]
	s_nop 2
	ds_read_b64_tr_b16 v[88:89], v192 offset:9280
	ds_read_b64_tr_b16 v[90:91], v192 offset:11584
	v_pk_mul_f32 v[98:99], v[62:63], v[108:109] op_sel_hi:[1,0]
	v_pk_mul_f32 v[96:97], v[60:61], v[108:109] op_sel_hi:[1,0]
	s_waitcnt lgkmcnt(2)
	v_mfma_f32_16x16x32_bf16 v[76:79], v[76:79], v[36:39], v[92:95]
	s_nop 2
	ds_read_b64_tr_b16 v[92:93], v192 offset:9312
	ds_read_b64_tr_b16 v[94:95], v192 offset:11616
	v_pk_mul_f32 v[106:107], v[86:87], v[108:109] op_sel_hi:[1,0]
	v_pk_mul_f32 v[104:105], v[84:85], v[108:109] op_sel_hi:[1,0]
	s_waitcnt lgkmcnt(2)
	v_mfma_f32_16x16x32_bf16 v[88:91], v[88:91], v[36:39], v[96:99]
	v_fmac_f32_e32 v130, v128, v108
	s_waitcnt lgkmcnt(0)
	v_mfma_f32_16x16x32_bf16 v[36:39], v[92:95], v[36:39], v[104:107]
	ds_read_b64_tr_b16 v[94:95], v193 offset:11520
	ds_read_b64_tr_b16 v[92:93], v193 offset:9216
	ds_read_b64_tr_b16 v[96:97], v193 offset:9248
	ds_read_b64_tr_b16 v[98:99], v193 offset:11552
	s_waitcnt lgkmcnt(2)
	v_mfma_f32_16x16x32_bf16 v[68:71], v[92:95], v[40:43], v[68:71]
	ds_read_b64_tr_b16 v[92:93], v193 offset:9280
	ds_read_b64_tr_b16 v[94:95], v193 offset:11584
	s_waitcnt lgkmcnt(0)
	v_mfma_f32_16x16x32_bf16 v[88:91], v[92:95], v[40:43], v[88:91]
	ds_read_b64_tr_b16 v[92:93], v193 offset:9312
	ds_read_b64_tr_b16 v[94:95], v193 offset:11616
	v_mfma_f32_16x16x32_bf16 v[76:79], v[96:99], v[40:43], v[76:79]
	s_waitcnt lgkmcnt(0)
	v_mfma_f32_16x16x32_bf16 v[108:111], v[92:95], v[40:43], v[36:39]

.LBB0_607:
	ds_read_b128 v[88:91], v191
	ds_read_b128 v[224:227], v191 offset:64
	ds_read_b128 v[228:231], v191 offset:2304
	ds_read_b128 v[232:235], v191 offset:2368
	ds_read_b128 v[236:239], v191 offset:4608
	ds_read_b128 v[240:243], v191 offset:4672
	ds_read_b128 v[244:247], v191 offset:6912
	ds_read_b128 v[182:185], v191 offset:6976
	v_mov_b32_e32 v130, v128
	v_mov_b32_e32 v219, v3
	s_waitcnt lgkmcnt(7)
	v_mfma_f32_16x16x32_bf16 v[40:43], v[88:91], v[4:7], v[40:43]
	s_waitcnt lgkmcnt(6)
	v_mfma_f32_16x16x32_bf16 v[40:43], v[224:227], v[8:11], v[40:43]
	s_waitcnt lgkmcnt(5)
	v_mfma_f32_16x16x32_bf16 v[36:39], v[228:231], v[4:7], v[36:39]
	s_waitcnt lgkmcnt(4)
	v_mfma_f32_16x16x32_bf16 v[36:39], v[232:235], v[8:11], v[36:39]
	s_waitcnt lgkmcnt(3)
	v_mfma_f32_16x16x32_bf16 v[76:79], v[236:239], v[4:7], v[76:79]
	s_waitcnt lgkmcnt(2)
	v_mfma_f32_16x16x32_bf16 v[76:79], v[240:243], v[8:11], v[76:79]
	s_nop 6
	s_waitcnt lgkmcnt(1)
	v_mfma_f32_16x16x32_bf16 v[68:71], v[244:247], v[4:7], v[68:71]
	s_waitcnt lgkmcnt(0)
	v_mfma_f32_16x16x32_bf16 v[68:71], v[182:185], v[8:11], v[68:71]
	v_max_f32_e32 v88, v42, v43
	v_max_f32_e32 v89, v38, v39
	v_max_f32_e32 v90, v76, v77
	v_max_f32_e32 v91, v78, v79
	s_nop 3
	v_max_f32_e32 v92, v70, v71
	v_max3_f32 v92, v68, v69, v92
	v_max3_f32 v88, v40, v41, v88
	v_max3_f32 v89, v36, v37, v89
	v_max3_f32 v90, v90, v91, v92
	v_max3_f32 v88, v88, v89, v90
	v_mov_b32_e32 v89, v88
	s_nop 1
	v_permlane32_swap_b32_e32 v88, v89
	v_max_f32_e32 v88, v88, v89
	v_mov_b32_e32 v89, v88
	s_nop 1
	v_permlane16_swap_b32_e32 v88, v89
	v_max3_f32 v220, v217, v88, v89
	v_sub_f32_e32 v41, v41, v220
	v_exp_f32_e32 v110, v41
	v_sub_f32_e32 v41, v42, v220
	v_sub_f32_e32 v42, v43, v220
	v_sub_f32_e32 v36, v36, v220
	v_exp_f32_e32 v111, v42
	v_exp_f32_e32 v42, v36
	v_sub_f32_e32 v36, v37, v220
	v_exp_f32_e32 v112, v36
	v_sub_f32_e32 v36, v38, v220
	v_exp_f32_e32 v43, v36
	v_sub_f32_e32 v36, v39, v220
	v_exp_f32_e32 v113, v36
	v_sub_f32_e32 v36, v76, v220
	v_exp_f32_e32 v76, v36
	v_sub_f32_e32 v36, v77, v220
	v_exp_f32_e32 v114, v36
	v_sub_f32_e32 v36, v78, v220
	v_exp_f32_e32 v77, v36
	v_sub_f32_e32 v36, v79, v220
	v_sub_f32_e32 v40, v40, v220
	v_exp_f32_e32 v115, v36
	v_sub_f32_e32 v36, v68, v220
	v_exp_f32_e32 v40, v40
	v_exp_f32_e32 v41, v41
	v_exp_f32_e32 v68, v36
	v_sub_f32_e32 v36, v69, v220
	v_exp_f32_e32 v78, v36
	v_sub_f32_e32 v36, v70, v220
	v_exp_f32_e32 v69, v36
	v_sub_f32_e32 v36, v71, v220
	v_exp_f32_e32 v79, v36
	v_pk_add_f32 v[36:37], v[42:43], v[40:41]
	v_pk_add_f32 v[38:39], v[112:113], v[110:111]
	v_pk_add_f32 v[36:37], v[76:77], v[36:37]
	v_pk_add_f32 v[38:39], v[114:115], v[38:39]
	v_pk_add_f32 v[36:37], v[68:69], v[36:37]
	v_pk_add_f32 v[38:39], v[78:79], v[38:39]
	v_sub_f32_e32 v88, v217, v220
	v_pk_add_f32 v[36:37], v[36:37], v[38:39]
	v_exp_f32_e32 v108, v88
	v_add_f32_e32 v131, v36, v37
	v_cvt_pk_bf16_f32 v36, v40, v110
	v_cvt_pk_bf16_f32 v37, v41, v111
	v_cvt_pk_bf16_f32 v38, v42, v112
	v_cvt_pk_bf16_f32 v39, v43, v113
	v_cvt_pk_bf16_f32 v40, v76, v114
	v_cvt_pk_bf16_f32 v41, v77, v115
	v_cvt_pk_bf16_f32 v42, v68, v78
	v_cvt_pk_bf16_f32 v43, v69, v79
	ds_read_b64_tr_b16 v[70:71], v192 offset:11520
	ds_read_b64_tr_b16 v[68:69], v192 offset:9216
	ds_read_b64_tr_b16 v[76:77], v192 offset:9248
	ds_read_b64_tr_b16 v[78:79], v192 offset:11552
	v_pk_mul_f32 v[90:91], v[66:67], v[108:109] op_sel_hi:[1,0]
	v_pk_mul_f32 v[88:89], v[64:65], v[108:109] op_sel_hi:[1,0]
	v_pk_mul_f32 v[94:95], v[74:75], v[108:109] op_sel_hi:[1,0]
	v_pk_mul_f32 v[92:93], v[72:73], v[108:109] op_sel_hi:[1,0]
	s_waitcnt lgkmcnt(2)
	v_mfma_f32_16x16x32_bf16 v[68:71], v[68:71], v[36:39], v[88:91]
	s_nop 2
	ds_read_b64_tr_b16 v[88:89], v192 offset:9280
	ds_read_b64_tr_b16 v[90:91], v192 offset:11584
	v_pk_mul_f32 v[98:99], v[82:83], v[108:109] op_sel_hi:[1,0]
	v_pk_mul_f32 v[96:97], v[80:81], v[108:109] op_sel_hi:[1,0]
	s_waitcnt lgkmcnt(2)
	v_mfma_f32_16x16x32_bf16 v[76:79], v[76:79], v[36:39], v[92:95]
	s_nop 2
	ds_read_b64_tr_b16 v[92:93], v192 offset:9312
	ds_read_b64_tr_b16 v[94:95], v192 offset:11616
	v_pk_mul_f32 v[106:107], v[102:103], v[108:109] op_sel_hi:[1,0]
	v_pk_mul_f32 v[104:105], v[100:101], v[108:109] op_sel_hi:[1,0]
	s_waitcnt lgkmcnt(2)
	v_mfma_f32_16x16x32_bf16 v[88:91], v[88:91], v[36:39], v[96:99]
	v_fmac_f32_e32 v131, v129, v108
	v_mov_b64_e32 v[110:111], v[86:87]
	v_mov_b64_e32 v[108:109], v[84:85]
	s_waitcnt lgkmcnt(0)
	v_mfma_f32_16x16x32_bf16 v[36:39], v[92:95], v[36:39], v[104:107]
	ds_read_b64_tr_b16 v[94:95], v193 offset:11520
	ds_read_b64_tr_b16 v[92:93], v193 offset:9216
	ds_read_b64_tr_b16 v[96:97], v193 offset:9248
	ds_read_b64_tr_b16 v[98:99], v193 offset:11552
	s_waitcnt lgkmcnt(2)
	v_mfma_f32_16x16x32_bf16 v[92:95], v[92:95], v[40:43], v[68:71]
	s_nop 2
	ds_read_b64_tr_b16 v[68:69], v193 offset:9280
	ds_read_b64_tr_b16 v[70:71], v193 offset:11584
	s_waitcnt lgkmcnt(0)
	v_mfma_f32_16x16x32_bf16 v[104:107], v[68:71], v[40:43], v[88:91]
	ds_read_b64_tr_b16 v[68:69], v193 offset:9312
	ds_read_b64_tr_b16 v[70:71], v193 offset:11616
	s_nop 0
	v_mov_b64_e32 v[90:91], v[62:63]
	v_mov_b64_e32 v[88:89], v[60:61]
	v_mfma_f32_16x16x32_bf16 v[96:99], v[96:99], v[40:43], v[76:79]
	s_waitcnt lgkmcnt(0)
	v_mfma_f32_16x16x32_bf16 v[112:115], v[68:71], v[40:43], v[36:39]
	v_mov_b64_e32 v[70:71], v[54:55]
	v_mov_b64_e32 v[78:79], v[58:59]
	v_mov_b64_e32 v[68:69], v[52:53]
	v_mov_b64_e32 v[76:77], v[56:57]

.LBB0_626:
	ds_read_b128 v[108:111], v191
	ds_read_b128 v[112:115], v191 offset:64
	ds_read_b128 v[224:227], v191 offset:2304
	ds_read_b128 v[228:231], v191 offset:2368
	ds_read_b128 v[232:235], v191 offset:4608
	ds_read_b128 v[236:239], v191 offset:4672
	ds_read_b128 v[240:243], v191 offset:6912
	ds_read_b128 v[244:247], v191 offset:6976
	s_waitcnt lgkmcnt(7)
	v_mfma_f32_16x16x32_bf16 v[68:71], v[108:111], v[4:7], v[68:71]
	v_mfma_f32_16x16x32_bf16 v[92:95], v[108:111], v[12:15], v[92:95]
	s_waitcnt lgkmcnt(6)
	v_mfma_f32_16x16x32_bf16 v[108:111], v[112:115], v[8:11], v[68:71]
	v_mfma_f32_16x16x32_bf16 v[68:71], v[112:115], v[16:19], v[92:95]
	s_nop 4
	s_waitcnt lgkmcnt(5)
	v_mfma_f32_16x16x32_bf16 v[36:39], v[224:227], v[4:7], v[36:39]
	v_mfma_f32_16x16x32_bf16 v[88:91], v[224:227], v[12:15], v[88:91]
	s_waitcnt lgkmcnt(4)
	v_mfma_f32_16x16x32_bf16 v[36:39], v[228:231], v[8:11], v[36:39]
	v_mfma_f32_16x16x32_bf16 v[92:95], v[228:231], v[16:19], v[88:91]
	s_nop 3
	s_waitcnt lgkmcnt(3)
	v_mfma_f32_16x16x32_bf16 v[76:79], v[232:235], v[4:7], v[76:79]
	v_mfma_f32_16x16x32_bf16 v[88:91], v[232:235], v[12:15], v[96:99]
	s_nop 2
	s_waitcnt lgkmcnt(2)
	v_mfma_f32_16x16x32_bf16 v[148:151], v[236:239], v[8:11], v[76:79]
	s_nop 2
	v_mfma_f32_16x16x32_bf16 v[96:99], v[236:239], v[16:19], v[88:91]
	s_nop 2
	s_waitcnt lgkmcnt(1)
	v_mfma_f32_16x16x32_bf16 v[40:43], v[240:243], v[4:7], v[40:43]
	v_mfma_f32_16x16x32_bf16 v[76:79], v[240:243], v[12:15], v[104:107]
	s_waitcnt lgkmcnt(0)
	v_mfma_f32_16x16x32_bf16 v[154:157], v[244:247], v[8:11], v[40:43]
	s_nop 4
	v_max_f32_e32 v40, v110, v111
	v_max_f32_e32 v41, v38, v39
	v_mfma_f32_16x16x32_bf16 v[104:107], v[244:247], v[16:19], v[76:79]
	v_max_f32_e32 v42, v148, v149
	v_max3_f32 v40, v108, v109, v40
	v_max_f32_e32 v43, v150, v151
	v_max_f32_e32 v76, v156, v157
	v_max3_f32 v76, v154, v155, v76
	v_max3_f32 v41, v36, v37, v41
	v_max3_f32 v42, v42, v43, v76
	v_max3_f32 v40, v40, v41, v42
	v_mov_b32_e32 v41, v40
	s_nop 1
	v_permlane32_swap_b32_e32 v40, v41
	v_max_f32_e32 v40, v40, v41
	v_mov_b32_e32 v41, v40
	s_nop 1
	v_permlane16_swap_b32_e32 v40, v41
	v_max3_f32 v220, v217, v40, v41
	v_sub_f32_e32 v40, v217, v220
	v_exp_f32_e32 v130, v40
	v_sub_f32_e32 v36, v36, v220
	v_exp_f32_e32 v133, v36
	v_sub_f32_e32 v36, v37, v220
	v_pk_mul_f32 v[88:89], v[64:65], v[130:131] op_sel_hi:[1,0]
	v_pk_mul_f32 v[64:65], v[80:81], v[130:131] op_sel_hi:[1,0]
	v_pk_mul_f32 v[90:91], v[66:67], v[130:131] op_sel_hi:[1,0]
	v_pk_mul_f32 v[66:67], v[82:83], v[130:131] op_sel_hi:[1,0]
	v_max_f32_e32 v80, v70, v71
	v_max_f32_e32 v81, v94, v95
	v_pk_mul_f32 v[40:41], v[100:101], v[130:131] op_sel_hi:[1,0]
	v_max_f32_e32 v82, v96, v97
	v_max_f32_e32 v83, v98, v99
	v_max_f32_e32 v100, v106, v107
	v_max3_f32 v100, v104, v105, v100
	v_max3_f32 v80, v68, v69, v80
	v_max3_f32 v81, v92, v93, v81
	v_max3_f32 v82, v82, v83, v100
	v_max3_f32 v80, v80, v81, v82
	v_mov_b32_e32 v81, v80
	s_nop 1
	v_permlane32_swap_b32_e32 v80, v81
	v_max_f32_e32 v80, v80, v81
	v_mov_b32_e32 v81, v80
	s_nop 1
	v_permlane16_swap_b32_e32 v80, v81
	v_max3_f32 v219, v3, v80, v81
	v_sub_f32_e32 v3, v3, v219
	v_exp_f32_e32 v222, v3
	v_sub_f32_e32 v3, v68, v219
	v_exp_f32_e32 v112, v3
	v_sub_f32_e32 v3, v69, v219
	v_pk_mul_f32 v[76:77], v[72:73], v[130:131] op_sel_hi:[1,0]
	v_sub_f32_e32 v72, v108, v220
	v_exp_f32_e32 v108, v3
	v_sub_f32_e32 v3, v70, v219
	v_exp_f32_e32 v113, v72
	v_sub_f32_e32 v72, v109, v220
	v_exp_f32_e32 v114, v3
	v_sub_f32_e32 v3, v71, v219
	v_exp_f32_e32 v109, v72
	v_sub_f32_e32 v72, v110, v220
	v_exp_f32_e32 v110, v3
	v_sub_f32_e32 v3, v92, v219
	v_exp_f32_e32 v132, v3
	v_sub_f32_e32 v3, v93, v219
	v_exp_f32_e32 v137, v36
	v_sub_f32_e32 v36, v38, v220
	v_exp_f32_e32 v136, v3
	v_sub_f32_e32 v3, v94, v219
	v_exp_f32_e32 v139, v36
	v_sub_f32_e32 v36, v39, v220
	v_exp_f32_e32 v138, v3
	v_sub_f32_e32 v3, v95, v219
	v_exp_f32_e32 v147, v36
	v_sub_f32_e32 v36, v148, v220
	v_exp_f32_e32 v146, v3
	v_sub_f32_e32 v3, v96, v219
	v_exp_f32_e32 v135, v36
	v_sub_f32_e32 v36, v149, v220
	v_exp_f32_e32 v134, v3
	v_sub_f32_e32 v3, v97, v219
	v_exp_f32_e32 v141, v36
	v_sub_f32_e32 v36, v150, v220
	v_exp_f32_e32 v140, v3
	v_sub_f32_e32 v3, v98, v219
	v_exp_f32_e32 v143, v36
	v_sub_f32_e32 v36, v151, v220
	v_exp_f32_e32 v142, v3
	v_sub_f32_e32 v3, v99, v219
	v_exp_f32_e32 v115, v72
	v_sub_f32_e32 v72, v111, v220
	v_exp_f32_e32 v149, v36
	v_sub_f32_e32 v36, v154, v220
	v_exp_f32_e32 v148, v3
	v_sub_f32_e32 v3, v104, v219
	v_exp_f32_e32 v111, v72
	v_exp_f32_e32 v151, v36
	v_sub_f32_e32 v36, v155, v220
	v_exp_f32_e32 v150, v3
	v_sub_f32_e32 v3, v105, v219
	v_exp_f32_e32 v153, v36
	v_sub_f32_e32 v36, v156, v220
	v_exp_f32_e32 v152, v3
	v_sub_f32_e32 v3, v106, v219
	v_exp_f32_e32 v155, v36
	v_sub_f32_e32 v36, v157, v220
	v_exp_f32_e32 v154, v3
	v_sub_f32_e32 v3, v107, v219
	v_exp_f32_e32 v157, v36
	v_exp_f32_e32 v156, v3
	v_pk_mul_f32 v[82:83], v[58:59], v[222:223] op_sel_hi:[1,0]
	v_pk_mul_f32 v[80:81], v[56:57], v[222:223] op_sel_hi:[1,0]
	v_pk_add_f32 v[56:57], v[132:133], v[112:113]
	v_pk_add_f32 v[58:59], v[136:137], v[108:109]
	v_pk_add_f32 v[68:69], v[138:139], v[114:115]
	v_pk_add_f32 v[70:71], v[146:147], v[110:111]
	v_pk_add_f32 v[56:57], v[134:135], v[56:57]
	v_pk_add_f32 v[58:59], v[140:141], v[58:59]
	v_pk_add_f32 v[68:69], v[142:143], v[68:69]
	v_pk_add_f32 v[70:71], v[148:149], v[70:71]
	v_pk_add_f32 v[56:57], v[150:151], v[56:57]
	v_pk_add_f32 v[58:59], v[152:153], v[58:59]
	v_pk_add_f32 v[68:69], v[154:155], v[68:69]
	v_pk_add_f32 v[70:71], v[156:157], v[70:71]
	v_pk_add_f32 v[56:57], v[56:57], v[58:59]
	v_pk_add_f32 v[58:59], v[68:69], v[70:71]
	v_pk_mul_f32 v[42:43], v[102:103], v[130:131] op_sel_hi:[1,0]
	v_pk_mul_f32 v[102:103], v[54:55], v[222:223] op_sel_hi:[1,0]
	v_pk_mul_f32 v[100:101], v[52:53], v[222:223] op_sel_hi:[1,0]
	v_pk_mul_f32 v[62:63], v[62:63], v[222:223] op_sel_hi:[1,0]
	v_pk_mul_f32 v[60:61], v[60:61], v[222:223] op_sel_hi:[1,0]
	v_pk_mul_f32 v[54:55], v[86:87], v[222:223] op_sel_hi:[1,0]
	v_pk_mul_f32 v[52:53], v[84:85], v[222:223] op_sel_hi:[1,0]
	v_mov_b32_e32 v223, v130
	v_pk_add_f32 v[56:57], v[56:57], v[58:59]
	v_pk_mul_f32 v[78:79], v[74:75], v[130:131] op_sel_hi:[1,0]
	v_cvt_pk_bf16_f32 v72, v113, v109
	v_cvt_pk_bf16_f32 v73, v115, v111
	v_cvt_pk_bf16_f32 v74, v133, v137
	v_cvt_pk_bf16_f32 v75, v139, v147
	v_cvt_pk_bf16_f32 v36, v135, v141
	v_cvt_pk_bf16_f32 v37, v143, v149
	v_cvt_pk_bf16_f32 v38, v151, v153
	v_cvt_pk_bf16_f32 v39, v155, v157
	v_pk_fma_f32 v[130:131], v[128:129], v[222:223], v[56:57]
	v_cvt_pk_bf16_f32 v68, v112, v108
	v_cvt_pk_bf16_f32 v69, v114, v110
	v_cvt_pk_bf16_f32 v70, v132, v136
	v_cvt_pk_bf16_f32 v71, v138, v146
	v_cvt_pk_bf16_f32 v56, v134, v140
	v_cvt_pk_bf16_f32 v57, v142, v148
	v_cvt_pk_bf16_f32 v58, v150, v152
	v_cvt_pk_bf16_f32 v59, v154, v156
	ds_read_b64_tr_b16 v[86:87], v192 offset:11520
	ds_read_b64_tr_b16 v[84:85], v192 offset:9216
	ds_read_b64_tr_b16 v[92:93], v192 offset:9248
	ds_read_b64_tr_b16 v[94:95], v192 offset:11552
	s_waitcnt lgkmcnt(0)
	v_mfma_f32_16x16x32_bf16 v[76:79], v[92:95], v[72:75], v[76:79]
	v_mfma_f32_16x16x32_bf16 v[80:83], v[92:95], v[68:71], v[80:83]
	ds_read_b64_tr_b16 v[92:93], v192 offset:9280
	ds_read_b64_tr_b16 v[94:95], v192 offset:11584
	s_waitcnt lgkmcnt(0)
	v_mfma_f32_16x16x32_bf16 v[64:67], v[92:95], v[72:75], v[64:67]
	v_mfma_f32_16x16x32_bf16 v[60:63], v[92:95], v[68:71], v[60:63]
	ds_read_b64_tr_b16 v[92:93], v192 offset:9312
	ds_read_b64_tr_b16 v[94:95], v192 offset:11616
	v_mfma_f32_16x16x32_bf16 v[88:91], v[84:87], v[72:75], v[88:91]
	v_mfma_f32_16x16x32_bf16 v[84:87], v[84:87], v[68:71], v[100:103]
	s_waitcnt lgkmcnt(0)
	v_mfma_f32_16x16x32_bf16 v[40:43], v[92:95], v[72:75], v[40:43]
	v_mfma_f32_16x16x32_bf16 v[52:55], v[92:95], v[68:71], v[52:55]
	ds_read_b64_tr_b16 v[70:71], v193 offset:11520
	ds_read_b64_tr_b16 v[68:69], v193 offset:9216
	ds_read_b64_tr_b16 v[72:73], v193 offset:9248
	ds_read_b64_tr_b16 v[74:75], v193 offset:11552
	s_waitcnt lgkmcnt(0)
	v_mfma_f32_16x16x32_bf16 v[96:99], v[72:75], v[36:39], v[76:79]
	v_mfma_f32_16x16x32_bf16 v[76:79], v[72:75], v[56:59], v[80:83]
	ds_read_b64_tr_b16 v[72:73], v193 offset:9280
	ds_read_b64_tr_b16 v[74:75], v193 offset:11584
	v_mfma_f32_16x16x32_bf16 v[92:95], v[68:71], v[36:39], v[88:91]
	s_waitcnt lgkmcnt(0)
	v_mfma_f32_16x16x32_bf16 v[88:91], v[72:75], v[56:59], v[60:63]
	s_nop 2
	ds_read_b64_tr_b16 v[60:61], v193 offset:9312
	ds_read_b64_tr_b16 v[62:63], v193 offset:11616
	v_mfma_f32_16x16x32_bf16 v[68:71], v[68:71], v[56:59], v[84:87]
	v_mfma_f32_16x16x32_bf16 v[104:107], v[72:75], v[36:39], v[64:67]
	s_waitcnt lgkmcnt(0)
	v_mfma_f32_16x16x32_bf16 v[112:115], v[60:63], v[36:39], v[40:43]
	v_mfma_f32_16x16x32_bf16 v[108:111], v[60:63], v[56:59], v[52:55]

.LBB0_638:
	ds_read_b128 v[60:63], v191 offset:18432
	ds_read_b128 v[224:227], v191 offset:18496
	ds_read_b128 v[228:231], v191 offset:20736
	ds_read_b128 v[232:235], v191 offset:20800
	ds_read_b128 v[236:239], v191 offset:23040
	ds_read_b128 v[240:243], v191 offset:23104
	ds_read_b128 v[244:247], v191 offset:25344
	ds_read_b128 v[182:185], v191 offset:25408
	v_mov_b32_e32 v129, v131
	s_waitcnt lgkmcnt(7)
	v_mfma_f32_16x16x32_bf16 v[48:51], v[60:63], v[12:15], v[48:51]
	s_waitcnt lgkmcnt(6)
	v_mfma_f32_16x16x32_bf16 v[48:51], v[224:227], v[16:19], v[48:51]
	s_nop 6
	s_waitcnt lgkmcnt(5)
	v_mfma_f32_16x16x32_bf16 v[44:47], v[228:231], v[12:15], v[44:47]
	s_waitcnt lgkmcnt(4)
	v_mfma_f32_16x16x32_bf16 v[44:47], v[232:235], v[16:19], v[44:47]
	s_waitcnt lgkmcnt(3)
	v_mfma_f32_16x16x32_bf16 v[56:59], v[236:239], v[12:15], v[56:59]
	s_waitcnt lgkmcnt(2)
	v_mfma_f32_16x16x32_bf16 v[56:59], v[240:243], v[16:19], v[56:59]
	s_waitcnt lgkmcnt(1)
	v_mfma_f32_16x16x32_bf16 v[52:55], v[244:247], v[12:15], v[52:55]
	s_waitcnt lgkmcnt(0)
	v_mfma_f32_16x16x32_bf16 v[52:55], v[182:185], v[16:19], v[52:55]
	v_max_f32_e32 v3, v50, v51
	v_max_f32_e32 v60, v46, v47
	s_nop 1
	v_max_f32_e32 v61, v56, v57
	v_max_f32_e32 v62, v58, v59
	s_nop 1
	v_max_f32_e32 v63, v54, v55
	v_max3_f32 v63, v52, v53, v63
	v_max3_f32 v3, v48, v49, v3
	v_max3_f32 v60, v44, v45, v60
	v_max3_f32 v61, v61, v62, v63
	v_max3_f32 v3, v3, v60, v61
	v_mov_b32_e32 v60, v3
	s_nop 1
	v_permlane32_swap_b32_e32 v3, v60
	v_max_f32_e32 v3, v3, v60
	v_mov_b32_e32 v60, v3
	s_nop 1
	v_permlane16_swap_b32_e32 v3, v60
	v_max3_f32 v217, v219, v3, v60
	v_sub_f32_e32 v3, v219, v217
	v_exp_f32_e32 v84, v3
	v_sub_f32_e32 v3, v48, v217
	v_exp_f32_e32 v48, v3
	v_sub_f32_e32 v3, v49, v217
	v_exp_f32_e32 v86, v3
	v_sub_f32_e32 v3, v50, v217
	v_exp_f32_e32 v49, v3
	v_sub_f32_e32 v3, v51, v217
	v_exp_f32_e32 v87, v3
	v_sub_f32_e32 v3, v44, v217
	v_exp_f32_e32 v50, v3
	v_sub_f32_e32 v3, v45, v217
	v_exp_f32_e32 v100, v3
	v_sub_f32_e32 v3, v46, v217
	v_exp_f32_e32 v51, v3
	v_sub_f32_e32 v3, v47, v217
	v_exp_f32_e32 v101, v3
	v_sub_f32_e32 v3, v56, v217
	v_exp_f32_e32 v56, v3
	v_sub_f32_e32 v3, v57, v217
	v_exp_f32_e32 v102, v3
	v_sub_f32_e32 v3, v58, v217
	v_exp_f32_e32 v57, v3
	v_sub_f32_e32 v3, v59, v217
	v_exp_f32_e32 v103, v3
	v_sub_f32_e32 v3, v52, v217
	v_exp_f32_e32 v52, v3
	v_sub_f32_e32 v3, v53, v217
	v_exp_f32_e32 v58, v3
	v_sub_f32_e32 v3, v54, v217
	v_exp_f32_e32 v53, v3
	v_sub_f32_e32 v3, v55, v217
	v_exp_f32_e32 v59, v3
	v_pk_add_f32 v[44:45], v[50:51], v[48:49]
	v_pk_add_f32 v[46:47], v[100:101], v[86:87]
	v_pk_add_f32 v[44:45], v[56:57], v[44:45]
	v_pk_add_f32 v[46:47], v[102:103], v[46:47]
	v_pk_add_f32 v[44:45], v[52:53], v[44:45]
	v_pk_add_f32 v[46:47], v[58:59], v[46:47]
	v_pk_mul_f32 v[62:63], v[70:71], v[84:85] op_sel_hi:[1,0]
	v_pk_add_f32 v[44:45], v[44:45], v[46:47]
	v_pk_mul_f32 v[60:61], v[68:69], v[84:85] op_sel_hi:[1,0]
	v_add_f32_e32 v128, v44, v45
	v_cvt_pk_bf16_f32 v44, v48, v86
	v_cvt_pk_bf16_f32 v45, v49, v87
	v_cvt_pk_bf16_f32 v46, v50, v100
	v_cvt_pk_bf16_f32 v47, v51, v101
	v_cvt_pk_bf16_f32 v48, v56, v102
	v_cvt_pk_bf16_f32 v49, v57, v103
	v_cvt_pk_bf16_f32 v50, v52, v58
	v_cvt_pk_bf16_f32 v51, v53, v59
	ds_read_b64_tr_b16 v[54:55], v192 offset:29952
	ds_read_b64_tr_b16 v[52:53], v192 offset:27648
	ds_read_b64_tr_b16 v[56:57], v192 offset:27680
	ds_read_b64_tr_b16 v[58:59], v192 offset:29984
	v_pk_mul_f32 v[66:67], v[78:79], v[84:85] op_sel_hi:[1,0]
	v_pk_mul_f32 v[64:65], v[76:77], v[84:85] op_sel_hi:[1,0]
	s_waitcnt lgkmcnt(2)
	v_mfma_f32_16x16x32_bf16 v[52:55], v[52:55], v[44:47], v[60:63]
	s_nop 2
	ds_read_b64_tr_b16 v[60:61], v192 offset:27712
	ds_read_b64_tr_b16 v[62:63], v192 offset:30016
	v_pk_mul_f32 v[74:75], v[90:91], v[84:85] op_sel_hi:[1,0]
	v_pk_mul_f32 v[72:73], v[88:89], v[84:85] op_sel_hi:[1,0]
	s_waitcnt lgkmcnt(2)
	v_mfma_f32_16x16x32_bf16 v[56:59], v[56:59], v[44:47], v[64:67]
	s_nop 2
	ds_read_b64_tr_b16 v[64:65], v192 offset:27744
	ds_read_b64_tr_b16 v[66:67], v192 offset:30048
	v_pk_mul_f32 v[82:83], v[110:111], v[84:85] op_sel_hi:[1,0]
	v_pk_mul_f32 v[80:81], v[108:109], v[84:85] op_sel_hi:[1,0]
	s_waitcnt lgkmcnt(2)
	v_mfma_f32_16x16x32_bf16 v[60:63], v[60:63], v[44:47], v[72:75]
	v_fmac_f32_e32 v128, v130, v84
	s_waitcnt lgkmcnt(0)
	v_mfma_f32_16x16x32_bf16 v[44:47], v[64:67], v[44:47], v[80:83]
	ds_read_b64_tr_b16 v[66:67], v193 offset:29952
	ds_read_b64_tr_b16 v[64:65], v193 offset:27648
	ds_read_b64_tr_b16 v[72:73], v193 offset:27680
	ds_read_b64_tr_b16 v[74:75], v193 offset:29984
	s_waitcnt lgkmcnt(2)
	v_mfma_f32_16x16x32_bf16 v[52:55], v[64:67], v[48:51], v[52:55]
	ds_read_b64_tr_b16 v[64:65], v193 offset:27712
	ds_read_b64_tr_b16 v[66:67], v193 offset:30016
	s_waitcnt lgkmcnt(0)
	v_mfma_f32_16x16x32_bf16 v[60:63], v[64:67], v[48:51], v[60:63]
	ds_read_b64_tr_b16 v[64:65], v193 offset:27744
	ds_read_b64_tr_b16 v[66:67], v193 offset:30048
	v_mfma_f32_16x16x32_bf16 v[56:59], v[72:75], v[48:51], v[56:59]
	s_waitcnt lgkmcnt(0)
	v_mfma_f32_16x16x32_bf16 v[64:67], v[64:67], v[48:51], v[44:47]

.LBB0_649:
	ds_read_b128 v[60:63], v191 offset:18432
	ds_read_b128 v[224:227], v191 offset:18496
	ds_read_b128 v[228:231], v191 offset:20736
	ds_read_b128 v[232:235], v191 offset:20800
	ds_read_b128 v[236:239], v191 offset:23040
	ds_read_b128 v[240:243], v191 offset:23104
	ds_read_b128 v[244:247], v191 offset:25344
	ds_read_b128 v[182:185], v191 offset:25408
	v_mov_b32_e32 v128, v130
	v_mov_b32_e32 v217, v219
	s_waitcnt lgkmcnt(7)
	v_mfma_f32_16x16x32_bf16 v[48:51], v[60:63], v[4:7], v[48:51]
	s_waitcnt lgkmcnt(6)
	v_mfma_f32_16x16x32_bf16 v[48:51], v[224:227], v[8:11], v[48:51]
	s_nop 6
	s_waitcnt lgkmcnt(5)
	v_mfma_f32_16x16x32_bf16 v[44:47], v[228:231], v[4:7], v[44:47]
	s_waitcnt lgkmcnt(4)
	v_mfma_f32_16x16x32_bf16 v[44:47], v[232:235], v[8:11], v[44:47]
	s_waitcnt lgkmcnt(3)
	v_mfma_f32_16x16x32_bf16 v[56:59], v[236:239], v[4:7], v[56:59]
	s_waitcnt lgkmcnt(2)
	v_mfma_f32_16x16x32_bf16 v[56:59], v[240:243], v[8:11], v[56:59]
	s_waitcnt lgkmcnt(1)
	v_mfma_f32_16x16x32_bf16 v[52:55], v[244:247], v[4:7], v[52:55]
	s_waitcnt lgkmcnt(0)
	v_mfma_f32_16x16x32_bf16 v[52:55], v[182:185], v[8:11], v[52:55]
	v_max_f32_e32 v3, v50, v51
	v_max_f32_e32 v60, v46, v47
	s_nop 1
	v_max_f32_e32 v61, v56, v57
	v_max_f32_e32 v62, v58, v59
	s_nop 1
	v_max_f32_e32 v63, v54, v55
	v_max3_f32 v63, v52, v53, v63
	v_max3_f32 v3, v48, v49, v3
	v_max3_f32 v60, v44, v45, v60
	v_max3_f32 v61, v61, v62, v63
	v_max3_f32 v3, v3, v60, v61
	v_mov_b32_e32 v60, v3
	s_nop 1
	v_permlane32_swap_b32_e32 v3, v60
	v_max_f32_e32 v3, v3, v60
	v_mov_b32_e32 v60, v3
	s_nop 1
	v_permlane16_swap_b32_e32 v3, v60
	v_max3_f32 v218, v220, v3, v60
	v_sub_f32_e32 v3, v220, v218
	v_exp_f32_e32 v84, v3
	v_sub_f32_e32 v3, v48, v218
	v_exp_f32_e32 v48, v3
	v_sub_f32_e32 v3, v49, v218
	v_exp_f32_e32 v86, v3
	v_sub_f32_e32 v3, v50, v218
	v_exp_f32_e32 v49, v3
	v_sub_f32_e32 v3, v51, v218
	v_exp_f32_e32 v87, v3
	v_sub_f32_e32 v3, v44, v218
	v_exp_f32_e32 v50, v3
	v_sub_f32_e32 v3, v45, v218
	v_exp_f32_e32 v100, v3
	v_sub_f32_e32 v3, v46, v218
	v_exp_f32_e32 v51, v3
	v_sub_f32_e32 v3, v47, v218
	v_exp_f32_e32 v101, v3
	v_sub_f32_e32 v3, v56, v218
	v_exp_f32_e32 v56, v3
	v_sub_f32_e32 v3, v57, v218
	v_exp_f32_e32 v102, v3
	v_sub_f32_e32 v3, v58, v218
	v_exp_f32_e32 v57, v3
	v_sub_f32_e32 v3, v59, v218
	v_exp_f32_e32 v103, v3
	v_sub_f32_e32 v3, v52, v218
	v_exp_f32_e32 v52, v3
	v_sub_f32_e32 v3, v53, v218
	v_exp_f32_e32 v58, v3
	v_sub_f32_e32 v3, v54, v218
	v_exp_f32_e32 v53, v3
	v_sub_f32_e32 v3, v55, v218
	v_exp_f32_e32 v59, v3
	v_pk_add_f32 v[44:45], v[50:51], v[48:49]
	v_pk_add_f32 v[46:47], v[100:101], v[86:87]
	v_pk_add_f32 v[44:45], v[56:57], v[44:45]
	v_pk_add_f32 v[46:47], v[102:103], v[46:47]
	v_pk_add_f32 v[44:45], v[52:53], v[44:45]
	v_pk_add_f32 v[46:47], v[58:59], v[46:47]
	v_pk_mul_f32 v[62:63], v[94:95], v[84:85] op_sel_hi:[1,0]
	v_pk_add_f32 v[44:45], v[44:45], v[46:47]
	v_pk_mul_f32 v[60:61], v[92:93], v[84:85] op_sel_hi:[1,0]
	v_add_f32_e32 v129, v44, v45
	v_cvt_pk_bf16_f32 v44, v48, v86
	v_cvt_pk_bf16_f32 v45, v49, v87
	v_cvt_pk_bf16_f32 v46, v50, v100
	v_cvt_pk_bf16_f32 v47, v51, v101
	v_cvt_pk_bf16_f32 v48, v56, v102
	v_cvt_pk_bf16_f32 v49, v57, v103
	v_cvt_pk_bf16_f32 v50, v52, v58
	v_cvt_pk_bf16_f32 v51, v53, v59
	ds_read_b64_tr_b16 v[54:55], v192 offset:29952
	ds_read_b64_tr_b16 v[52:53], v192 offset:27648
	ds_read_b64_tr_b16 v[56:57], v192 offset:27680
	ds_read_b64_tr_b16 v[58:59], v192 offset:29984
	v_pk_mul_f32 v[66:67], v[98:99], v[84:85] op_sel_hi:[1,0]
	v_pk_mul_f32 v[64:65], v[96:97], v[84:85] op_sel_hi:[1,0]
	s_waitcnt lgkmcnt(2)
	v_mfma_f32_16x16x32_bf16 v[52:55], v[52:55], v[44:47], v[60:63]
	s_nop 2
	ds_read_b64_tr_b16 v[60:61], v192 offset:27712
	ds_read_b64_tr_b16 v[62:63], v192 offset:30016
	v_pk_mul_f32 v[74:75], v[106:107], v[84:85] op_sel_hi:[1,0]
	v_pk_mul_f32 v[72:73], v[104:105], v[84:85] op_sel_hi:[1,0]
	s_waitcnt lgkmcnt(2)
	v_mfma_f32_16x16x32_bf16 v[56:59], v[56:59], v[44:47], v[64:67]
	s_nop 2
	ds_read_b64_tr_b16 v[64:65], v192 offset:27744
	ds_read_b64_tr_b16 v[66:67], v192 offset:30048
	v_pk_mul_f32 v[82:83], v[114:115], v[84:85] op_sel_hi:[1,0]
	v_pk_mul_f32 v[80:81], v[112:113], v[84:85] op_sel_hi:[1,0]
	s_waitcnt lgkmcnt(2)
	v_mfma_f32_16x16x32_bf16 v[60:63], v[60:63], v[44:47], v[72:75]
	v_fmac_f32_e32 v129, v131, v84
	s_waitcnt lgkmcnt(0)
	v_mfma_f32_16x16x32_bf16 v[44:47], v[64:67], v[44:47], v[80:83]
	ds_read_b64_tr_b16 v[66:67], v193 offset:29952
	ds_read_b64_tr_b16 v[64:65], v193 offset:27648
	s_nop 0
	ds_read_b64_tr_b16 v[80:81], v193 offset:27680
	ds_read_b64_tr_b16 v[82:83], v193 offset:29984
	s_waitcnt lgkmcnt(2)
	v_mfma_f32_16x16x32_bf16 v[72:75], v[64:67], v[48:51], v[52:55]
	s_nop 2
	ds_read_b64_tr_b16 v[52:53], v193 offset:27712
	ds_read_b64_tr_b16 v[54:55], v193 offset:30016
	v_mov_b64_e32 v[64:65], v[108:109]
	v_mov_b64_e32 v[66:67], v[110:111]
	s_waitcnt lgkmcnt(0)
	v_mfma_f32_16x16x32_bf16 v[84:87], v[52:55], v[48:51], v[60:63]
	ds_read_b64_tr_b16 v[52:53], v193 offset:27744
	ds_read_b64_tr_b16 v[54:55], v193 offset:30048
	s_nop 0
	v_mov_b64_e32 v[60:61], v[88:89]
	v_mov_b64_e32 v[62:63], v[90:91]
	v_mfma_f32_16x16x32_bf16 v[80:83], v[80:83], v[48:51], v[56:59]
	s_waitcnt lgkmcnt(0)
	v_mfma_f32_16x16x32_bf16 v[100:103], v[52:55], v[48:51], v[44:47]
	v_mov_b64_e32 v[52:53], v[68:69]
	v_mov_b64_e32 v[56:57], v[76:77]
	v_mov_b64_e32 v[54:55], v[70:71]
	v_mov_b64_e32 v[58:59], v[78:79]
